# speedup vs baseline: 1.0046x; 1.0046x over previous
.LBB0_19:
	s_or_b64 exec, exec, s[2:3]
	v_mul_u32_u24_e32 v14, 0x52800, v11
	s_waitcnt vmcnt(0)
	v_cvt_pk_f16_f32 v9, v8, v9
	v_cvt_pk_f16_f32 v8, v6, v7
	v_cvt_pk_f16_f32 v6, v2, v3
	s_waitcnt lgkmcnt(0)
	v_lshl_add_u64 v[2:3], s[0:1], 0, v[14:15]
	v_ashrrev_i32_e32 v1, 2, v1
	v_ashrrev_i32_e32 v11, 31, v10
	s_movk_i32 s0, 0x210
	v_cvt_pk_f16_f32 v7, v4, v5
	v_mad_i64_i32 v[4:5], s[0:1], v1, s0, v[10:11]
	v_lshlrev_b64 v[4:5], 6, v[4:5]
	v_lshlrev_b32_e32 v0, 4, v0
	v_lshl_add_u64 v[2:3], v[2:3], 0, v[4:5]
	v_and_b32_e32 v14, 48, v0
	v_lshl_add_u64 v[0:1], v[2:3], 0, v[14:15]
	global_store_dwordx4 v[0:1], v[6:9], off
	s_endpgm
	.p2align	8

_ZN12_GLOBAL__N_17k_finalEPKfS1_Pf:
	s_load_dwordx4 s[8:11], s[0:1], 0x0
	s_load_dwordx2 s[4:5], s[0:1], 0x10
	v_lshl_or_b32 v4, s2, 8, v0
	v_ashrrev_i32_e32 v5, 31, v4
	v_lshlrev_b64 v[36:37], 4, v[4:5]
	s_waitcnt lgkmcnt(0)
	v_lshl_add_u64 v[32:33], s[8:9], 0, v[36:37]
	s_mov_b32 s0, 0x80000
	v_add_co_u32_e32 v12, vcc, s0, v32
	s_mov_b32 s0, 0x100000
	s_nop 0
	v_addc_co_u32_e32 v13, vcc, 0, v33, vcc
	v_add_co_u32_e32 v20, vcc, s0, v32
	s_mov_b32 s0, 0x180000
	s_nop 0
	v_addc_co_u32_e32 v21, vcc, 0, v33, vcc
	v_add_co_u32_e32 v22, vcc, s0, v32
	v_lshlrev_b32_e32 v0, 4, v0
	s_nop 0
	v_addc_co_u32_e32 v23, vcc, 0, v33, vcc
	s_mov_b32 s0, 0x200000
	v_and_b32_e32 v0, 16, v0
	v_add_co_u32_e32 v28, vcc, s0, v32
	global_load_dwordx4 v[0:3], v0, s[10:11]
	s_nop 0
	v_addc_co_u32_e32 v29, vcc, 0, v33, vcc
	s_mov_b32 s0, 0x280000
	global_load_dwordx4 v[4:7], v[32:33], off
	global_load_dwordx4 v[8:11], v[12:13], off
	v_add_co_u32_e32 v30, vcc, s0, v32
	s_mov_b32 s0, 0x300000
	s_nop 0
	v_addc_co_u32_e32 v31, vcc, 0, v33, vcc
	global_load_dwordx4 v[12:15], v[20:21], off
	global_load_dwordx4 v[16:19], v[22:23], off
	s_nop 0
	global_load_dwordx4 v[20:23], v[28:29], off
	global_load_dwordx4 v[24:27], v[30:31], off
	v_add_co_u32_e32 v28, vcc, s0, v32
	s_waitcnt vmcnt(5)
	v_pk_add_f32 v[2:3], v[2:3], v[6:7]
	v_addc_co_u32_e32 v29, vcc, 0, v33, vcc
	v_add_co_u32_e32 v32, vcc, 0x380000, v32
	global_load_dwordx4 v[28:31], v[28:29], off
	s_nop 0
	v_addc_co_u32_e32 v33, vcc, 0, v33, vcc
	global_load_dwordx4 v[32:35], v[32:33], off
	v_pk_add_f32 v[0:1], v[0:1], v[4:5]
	s_waitcnt vmcnt(6)
	v_pk_add_f32 v[2:3], v[2:3], v[10:11]
	v_pk_add_f32 v[0:1], v[0:1], v[8:9]
	s_waitcnt vmcnt(5)
	v_pk_add_f32 v[2:3], v[2:3], v[14:15]
	v_pk_add_f32 v[0:1], v[0:1], v[12:13]
	s_waitcnt vmcnt(4)
	v_pk_add_f32 v[2:3], v[2:3], v[18:19]
	v_pk_add_f32 v[0:1], v[0:1], v[16:17]
	s_waitcnt vmcnt(3)
	v_pk_add_f32 v[2:3], v[2:3], v[22:23]
	v_pk_add_f32 v[0:1], v[0:1], v[20:21]
	s_waitcnt vmcnt(2)
	v_pk_add_f32 v[2:3], v[2:3], v[26:27]
	v_pk_add_f32 v[0:1], v[0:1], v[24:25]
	v_lshl_add_u64 v[4:5], s[4:5], 0, v[36:37]
	s_waitcnt vmcnt(1)
	v_pk_add_f32 v[2:3], v[2:3], v[30:31]
	v_pk_add_f32 v[0:1], v[0:1], v[28:29]
	s_waitcnt vmcnt(0)
	v_pk_add_f32 v[2:3], v[2:3], v[34:35]
	v_pk_add_f32 v[0:1], v[0:1], v[32:33]
	global_store_dwordx4 v[4:5], v[0:3], off
	s_endpgm
	.p2align	8

.LBB2_8:
	s_or_b64 exec, exec, s[2:3]
	v_and_b32_e32 v1, 56, v1
	v_or_b32_e32 v12, s8, v93
	s_lshl_b32 s2, s9, 1
	v_lshl_add_u32 v0, v1, 2, 0
	s_add_u32 s0, s0, s2
	v_mad_u64_u32 v[18:19], s[2:3], v12, s4, v[0:1]
	ds_read_b128 v[4:7], v18 offset:272
	ds_read_b128 v[8:11], v18 offset:288
	v_add_u32_e32 v20, s5, v12
	s_addc_u32 s1, s1, 0
	v_lshlrev_b32_e32 v2, 1, v1
	v_mov_b32_e32 v3, 0
	s_waitcnt lgkmcnt(0)
	v_cvt_pk_f16_f32 v11, v10, v11
	v_cvt_pk_f16_f32 v10, v8, v9
	v_cvt_pk_f16_f32 v9, v6, v7
	v_cvt_pk_f16_f32 v8, v4, v5
	ds_read_b128 v[4:7], v18 offset:2448
	ds_read_b128 v[12:15], v18 offset:2464
	v_ashrrev_i32_e32 v21, 31, v20
	v_lshl_add_u64 v[2:3], s[0:1], 0, v[2:3]
	v_lshlrev_b64 v[16:17], 10, v[20:21]
	v_lshl_add_u64 v[16:17], v[2:3], 0, v[16:17]
	global_store_dwordx4 v[16:17], v[8:11], off nt
	s_waitcnt lgkmcnt(1)
	v_cvt_pk_f16_f32 v7, v6, v7
	v_cvt_pk_f16_f32 v6, v4, v5
	s_waitcnt lgkmcnt(0)
	v_cvt_pk_f16_f32 v9, v14, v15
	v_cvt_pk_f16_f32 v8, v12, v13
	v_add_u32_e32 v4, 8, v20
	ds_read_b128 v[10:13], v18 offset:4624
	ds_read_b128 v[14:17], v18 offset:4640
	v_ashrrev_i32_e32 v5, 31, v4
	v_lshlrev_b64 v[4:5], 10, v[4:5]
	v_lshl_add_u64 v[4:5], v[2:3], 0, v[4:5]
	global_store_dwordx4 v[4:5], v[6:9], off nt
	s_waitcnt lgkmcnt(1)
	v_cvt_pk_f16_f32 v5, v12, v13
	v_cvt_pk_f16_f32 v4, v10, v11
	s_waitcnt lgkmcnt(0)
	v_cvt_pk_f16_f32 v7, v16, v17
	v_cvt_pk_f16_f32 v6, v14, v15
	v_add_u32_e32 v16, 16, v20
	ds_read_b128 v[8:11], v18 offset:6800
	ds_read_b128 v[12:15], v18 offset:6816
	v_ashrrev_i32_e32 v17, 31, v16
	v_lshlrev_b64 v[16:17], 10, v[16:17]
	v_lshl_add_u64 v[16:17], v[2:3], 0, v[16:17]
	global_store_dwordx4 v[16:17], v[4:7], off nt
	v_add_u32_e32 v16, 24, v20
	v_ashrrev_i32_e32 v17, 31, v16
	s_waitcnt lgkmcnt(0)
	v_cvt_pk_f16_f32 v7, v14, v15
	v_cvt_pk_f16_f32 v6, v12, v13
	v_cvt_pk_f16_f32 v5, v10, v11
	v_cvt_pk_f16_f32 v4, v8, v9
	ds_read_b128 v[8:11], v18 offset:8976
	ds_read_b128 v[12:15], v18 offset:8992
	v_lshlrev_b64 v[16:17], 10, v[16:17]
	v_lshl_add_u64 v[16:17], v[2:3], 0, v[16:17]
	global_store_dwordx4 v[16:17], v[4:7], off nt
	v_add_u32_e32 v16, 32, v20
	v_ashrrev_i32_e32 v17, 31, v16
	s_waitcnt lgkmcnt(0)
	v_cvt_pk_f16_f32 v7, v14, v15
	v_cvt_pk_f16_f32 v6, v12, v13
	v_cvt_pk_f16_f32 v5, v10, v11
	v_cvt_pk_f16_f32 v4, v8, v9
	ds_read_b128 v[8:11], v18 offset:11152
	ds_read_b128 v[12:15], v18 offset:11168
	v_lshlrev_b64 v[16:17], 10, v[16:17]
	v_lshl_add_u64 v[16:17], v[2:3], 0, v[16:17]
	global_store_dwordx4 v[16:17], v[4:7], off nt
	v_add_u32_e32 v16, 40, v20
	v_ashrrev_i32_e32 v17, 31, v16
	s_waitcnt lgkmcnt(0)
	v_cvt_pk_f16_f32 v7, v14, v15
	v_cvt_pk_f16_f32 v6, v12, v13
	v_cvt_pk_f16_f32 v5, v10, v11
	v_cvt_pk_f16_f32 v4, v8, v9
	ds_read_b128 v[8:11], v18 offset:13328
	ds_read_b128 v[12:15], v18 offset:13344
	v_lshlrev_b64 v[16:17], 10, v[16:17]
	v_lshl_add_u64 v[16:17], v[2:3], 0, v[16:17]
	global_store_dwordx4 v[16:17], v[4:7], off nt
	v_add_u32_e32 v16, 48, v20
	v_ashrrev_i32_e32 v17, 31, v16
	s_waitcnt lgkmcnt(0)
	v_cvt_pk_f16_f32 v7, v14, v15
	v_cvt_pk_f16_f32 v6, v12, v13
	v_cvt_pk_f16_f32 v5, v10, v11
	v_cvt_pk_f16_f32 v4, v8, v9
	ds_read_b128 v[8:11], v18 offset:15504
	ds_read_b128 v[12:15], v18 offset:15520
	v_lshlrev_b64 v[16:17], 10, v[16:17]
	v_lshl_add_u64 v[16:17], v[2:3], 0, v[16:17]
	global_store_dwordx4 v[16:17], v[4:7], off nt
	s_mul_i32 s0, s8, 0x110
	s_add_i32 s0, s0, 0
	s_waitcnt lgkmcnt(1)
	v_cvt_pk_f16_f32 v4, v8, v9
	v_add_u32_e32 v8, 56, v20
	v_ashrrev_i32_e32 v9, 31, v8
	v_lshlrev_b64 v[8:9], 10, v[8:9]
	v_lshlrev_b32_e32 v1, 2, v94
	s_waitcnt lgkmcnt(0)
	v_cvt_pk_f16_f32 v7, v14, v15
	v_cvt_pk_f16_f32 v6, v12, v13
	v_cvt_pk_f16_f32 v5, v10, v11
	v_lshl_add_u64 v[8:9], v[2:3], 0, v[8:9]
	v_add_u32_e32 v90, s0, v1
	global_store_dwordx4 v[8:9], v[4:7], off nt
	ds_read2_b32 v[4:5], v90 offset0:68 offset1:136
	v_add_u32_e32 v91, 0x200, v90
	ds_read2_b32 v[6:7], v91 offset0:76 offset1:144
	v_add_u32_e32 v92, 0x400, v90
	ds_read2_b32 v[8:9], v92 offset0:84 offset1:152
	v_add_u32_e32 v94, 0x600, v90
	s_waitcnt lgkmcnt(2)
	v_add_f32_e32 v68, 0, v4
	ds_read2_b32 v[10:11], v94 offset0:92 offset1:160
	v_add_f32_e32 v68, v68, v5
	v_add_u32_e32 v95, 0x800, v90
	s_waitcnt lgkmcnt(2)
	v_add_f32_e32 v68, v68, v6
	ds_read2_b32 v[12:13], v95 offset0:100 offset1:168
	v_add_f32_e32 v68, v68, v7
	v_add_u32_e32 v96, 0xa00, v90
	s_waitcnt lgkmcnt(2)
	v_add_f32_e32 v68, v68, v8
	ds_read2_b32 v[14:15], v96 offset0:108 offset1:176
	v_add_f32_e32 v68, v68, v9
	v_add_u32_e32 v97, 0xc00, v90
	s_waitcnt lgkmcnt(2)
	v_add_f32_e32 v68, v68, v10
	ds_read2_b32 v[16:17], v97 offset0:116 offset1:184
	v_add_f32_e32 v68, v68, v11
	v_add_u32_e32 v98, 0xe00, v90
	s_waitcnt lgkmcnt(2)
	v_add_f32_e32 v68, v68, v12
	ds_read2_b32 v[18:19], v98 offset0:124 offset1:192
	v_add_f32_e32 v68, v68, v13
	v_add_u32_e32 v99, 0x1000, v90
	s_waitcnt lgkmcnt(2)
	v_add_f32_e32 v68, v68, v14
	ds_read2_b32 v[20:21], v99 offset0:132 offset1:200
	v_add_f32_e32 v68, v68, v15
	s_waitcnt lgkmcnt(2)
	v_add_f32_e32 v68, v68, v16
	v_add_u32_e32 v100, 0x1400, v90
	v_add_f32_e32 v68, v68, v17
	ds_read2_b32 v[22:23], v100 offset0:12 offset1:80
	ds_read2_b32 v[24:25], v100 offset0:148 offset1:216
	s_waitcnt lgkmcnt(3)
	v_add_f32_e32 v68, v68, v18
	v_add_f32_e32 v68, v68, v19
	s_waitcnt lgkmcnt(2)
	v_add_f32_e32 v68, v68, v20
	v_add_u32_e32 v101, 0x1800, v90
	v_add_f32_e32 v68, v68, v21
	ds_read2_b32 v[26:27], v101 offset0:28 offset1:96
	ds_read2_b32 v[28:29], v101 offset0:164 offset1:232
	s_waitcnt lgkmcnt(3)
	v_add_f32_e32 v68, v68, v22
	v_add_f32_e32 v68, v68, v23
	s_waitcnt lgkmcnt(2)
	v_add_f32_e32 v68, v68, v24
	v_add_u32_e32 v102, 0x1c00, v90
	v_add_f32_e32 v68, v68, v25
	ds_read2_b32 v[30:31], v102 offset0:44 offset1:112
	ds_read2_b32 v[32:33], v102 offset0:180 offset1:248
	s_waitcnt lgkmcnt(3)
	v_add_f32_e32 v68, v68, v26
	v_add_f32_e32 v68, v68, v27
	v_add_u32_e32 v103, 0x2000, v90
	s_waitcnt lgkmcnt(2)
	v_add_f32_e32 v68, v68, v28
	ds_read2_b32 v[34:35], v103 offset0:60 offset1:128
	v_add_f32_e32 v68, v68, v29
	v_add_u32_e32 v104, 0x2200, v90
	s_waitcnt lgkmcnt(2)
	v_add_f32_e32 v68, v68, v30
	ds_read2_b32 v[36:37], v104 offset0:68 offset1:136
	v_add_f32_e32 v68, v68, v31
	v_add_u32_e32 v105, 0x2400, v90
	s_waitcnt lgkmcnt(2)
	v_add_f32_e32 v68, v68, v32
	ds_read2_b32 v[38:39], v105 offset0:76 offset1:144
	v_add_f32_e32 v68, v68, v33
	v_add_u32_e32 v106, 0x2600, v90
	s_waitcnt lgkmcnt(2)
	v_add_f32_e32 v68, v68, v34
	ds_read2_b32 v[40:41], v106 offset0:84 offset1:152
	v_add_f32_e32 v68, v68, v35
	v_add_u32_e32 v107, 0x2800, v90
	s_waitcnt lgkmcnt(2)
	v_add_f32_e32 v68, v68, v36
	ds_read2_b32 v[42:43], v107 offset0:92 offset1:160
	v_add_f32_e32 v68, v68, v37
	v_add_u32_e32 v108, 0x2a00, v90
	s_waitcnt lgkmcnt(2)
	v_add_f32_e32 v68, v68, v38
	ds_read2_b32 v[44:45], v108 offset0:100 offset1:168
	v_add_f32_e32 v68, v68, v39
	v_add_u32_e32 v109, 0x2c00, v90
	s_waitcnt lgkmcnt(2)
	v_add_f32_e32 v68, v68, v40
	ds_read2_b32 v[46:47], v109 offset0:108 offset1:176
	v_add_f32_e32 v68, v68, v41
	v_add_u32_e32 v110, 0x2e00, v90
	s_waitcnt lgkmcnt(2)
	v_add_f32_e32 v68, v68, v42
	ds_read2_b32 v[48:49], v110 offset0:116 offset1:184
	v_add_f32_e32 v68, v68, v43
	v_add_u32_e32 v111, 0x3000, v90
	s_waitcnt lgkmcnt(2)
	v_add_f32_e32 v68, v68, v44
	ds_read2_b32 v[50:51], v111 offset0:124 offset1:192
	v_add_f32_e32 v68, v68, v45
	s_waitcnt lgkmcnt(2)
	v_add_f32_e32 v68, v68, v46
	v_add_u32_e32 v112, 0x3400, v90
	v_add_f32_e32 v68, v68, v47
	ds_read2_b32 v[52:53], v112 offset0:4 offset1:72
	ds_read2_b32 v[54:55], v112 offset0:140 offset1:208
	s_waitcnt lgkmcnt(3)
	v_add_f32_e32 v68, v68, v48
	v_add_f32_e32 v68, v68, v49
	s_waitcnt lgkmcnt(2)
	v_add_f32_e32 v68, v68, v50
	v_add_u32_e32 v113, 0x3800, v90
	v_add_f32_e32 v68, v68, v51
	ds_read2_b32 v[56:57], v113 offset0:20 offset1:88
	ds_read2_b32 v[58:59], v113 offset0:156 offset1:224
	s_waitcnt lgkmcnt(3)
	v_add_f32_e32 v68, v68, v52
	v_add_f32_e32 v68, v68, v53
	s_waitcnt lgkmcnt(2)
	v_add_f32_e32 v68, v68, v54
	v_add_u32_e32 v114, 0x3c00, v90
	v_add_f32_e32 v68, v68, v55
	ds_read2_b32 v[60:61], v114 offset0:36 offset1:104
	ds_read2_b32 v[62:63], v114 offset0:172 offset1:240
	s_waitcnt lgkmcnt(3)
	v_add_f32_e32 v68, v68, v56
	v_add_f32_e32 v68, v68, v57
	v_add_u32_e32 v115, 0x4000, v90
	s_waitcnt lgkmcnt(2)
	v_add_f32_e32 v68, v68, v58
	ds_read2_b32 v[64:65], v115 offset0:52 offset1:120
	v_add_f32_e32 v68, v68, v59
	v_add_u32_e32 v116, 0x4200, v90
	s_waitcnt lgkmcnt(2)
	v_add_f32_e32 v68, v68, v60
	ds_read2_b32 v[66:67], v116 offset0:60 offset1:128
	v_add_f32_e32 v68, v68, v61
	s_waitcnt lgkmcnt(2)
	v_add_f32_e32 v68, v68, v62
	v_add_f32_e32 v68, v68, v63
	s_waitcnt lgkmcnt(1)
	v_add_f32_e32 v68, v68, v64
	v_add_f32_e32 v68, v68, v65
	s_lshl_b32 s0, s8, 2
	s_add_i32 s1, 0, 0x22110
	s_waitcnt lgkmcnt(0)
	v_add_f32_e32 v68, v68, v66
	s_add_i32 s0, s1, s0
	v_add_f32_e32 v68, v68, v67
	v_add_u32_e32 v69, s0, v1
	v_add_u32_e32 v1, s1, v1
	ds_write_b32 v69, v68
	s_waitcnt lgkmcnt(0)
	s_barrier
	ds_read2st64_b32 v[68:69], v1 offset1:1
	s_cmpk_gt_u32 s20, 0x7f
	v_cndmask_b32_e64 v117, 1.0, 0, s[6:7]
	ds_read2st64_b32 v[70:71], v1 offset0:2 offset1:3
	ds_read2st64_b32 v[88:89], v1 offset0:4 offset1:5
	ds_read_b32 v1, v1 offset:1536
	s_cselect_b64 s[0:1], -1, 0
	s_cmpk_gt_u32 s20, 0xbf
	s_waitcnt lgkmcnt(3)
	v_fma_f32 v68, v117, v68, 0
	v_cndmask_b32_e64 v117, 0, 1.0, s[0:1]
	s_cselect_b64 s[0:1], -1, 0
	s_cmpk_gt_u32 s20, 0xff
	v_fmac_f32_e32 v68, v117, v69
	v_cndmask_b32_e64 v69, 0, 1.0, s[0:1]
	s_cselect_b64 s[0:1], -1, 0
	s_cmpk_gt_u32 s20, 0x13f
	s_waitcnt lgkmcnt(2)
	v_fmac_f32_e32 v68, v69, v70
	v_cndmask_b32_e64 v69, 0, 1.0, s[0:1]
	s_cselect_b64 s[0:1], -1, 0
	s_cmpk_gt_u32 s20, 0x17f
	v_fmac_f32_e32 v68, v69, v71
	v_cndmask_b32_e64 v69, 0, 1.0, s[0:1]
	s_cselect_b64 s[0:1], -1, 0
	s_cmpk_gt_u32 s20, 0x1bf
	s_waitcnt lgkmcnt(1)
	v_fmac_f32_e32 v68, v69, v88
	v_cndmask_b32_e64 v69, 0, 1.0, s[0:1]
	s_cselect_b64 s[0:1], -1, 0
	v_fmac_f32_e32 v68, v69, v89
	v_cndmask_b32_e64 v69, 0, 1.0, s[0:1]
	s_waitcnt lgkmcnt(0)
	v_fmac_f32_e32 v68, v69, v1
	v_add_f32_e32 v1, v68, v4
	v_add_f32_e32 v4, v1, v5
	ds_write2_b32 v90, v1, v4 offset0:68 offset1:136
	v_add_f32_e32 v1, v4, v6
	v_add_f32_e32 v4, v1, v7
	ds_write2_b32 v91, v1, v4 offset0:76 offset1:144
	v_add_f32_e32 v1, v4, v8
	v_add_f32_e32 v4, v1, v9
	ds_write2_b32 v92, v1, v4 offset0:84 offset1:152
	v_add_f32_e32 v1, v4, v10
	v_add_f32_e32 v4, v1, v11
	ds_write2_b32 v94, v1, v4 offset0:92 offset1:160
	v_add_f32_e32 v1, v4, v12
	v_add_f32_e32 v4, v1, v13
	ds_write2_b32 v95, v1, v4 offset0:100 offset1:168
	v_add_f32_e32 v1, v4, v14
	v_add_f32_e32 v4, v1, v15
	ds_write2_b32 v96, v1, v4 offset0:108 offset1:176
	v_add_f32_e32 v1, v4, v16
	v_add_f32_e32 v4, v1, v17
	ds_write2_b32 v97, v1, v4 offset0:116 offset1:184
	v_add_f32_e32 v1, v4, v18
	v_add_f32_e32 v4, v1, v19
	ds_write2_b32 v98, v1, v4 offset0:124 offset1:192
	v_add_f32_e32 v1, v4, v20
	v_add_f32_e32 v4, v1, v21
	ds_write2_b32 v99, v1, v4 offset0:132 offset1:200
	v_add_f32_e32 v1, v4, v22
	v_add_f32_e32 v4, v1, v23
	ds_write2_b32 v100, v1, v4 offset0:12 offset1:80
	v_add_f32_e32 v1, v4, v24
	v_add_f32_e32 v4, v1, v25
	ds_write2_b32 v100, v1, v4 offset0:148 offset1:216
	v_add_f32_e32 v1, v4, v26
	v_add_f32_e32 v4, v1, v27
	ds_write2_b32 v101, v1, v4 offset0:28 offset1:96
	v_add_f32_e32 v1, v4, v28
	v_add_f32_e32 v4, v1, v29
	ds_write2_b32 v101, v1, v4 offset0:164 offset1:232
	v_add_f32_e32 v1, v4, v30
	v_add_f32_e32 v4, v1, v31
	ds_write2_b32 v102, v1, v4 offset0:44 offset1:112
	v_add_f32_e32 v1, v4, v32
	v_add_f32_e32 v4, v1, v33
	ds_write2_b32 v102, v1, v4 offset0:180 offset1:248
	v_add_f32_e32 v1, v4, v34
	v_add_f32_e32 v4, v1, v35
	ds_write2_b32 v103, v1, v4 offset0:60 offset1:128
	v_add_f32_e32 v1, v4, v36
	v_add_f32_e32 v4, v1, v37
	ds_write2_b32 v104, v1, v4 offset0:68 offset1:136
	v_add_f32_e32 v1, v4, v38
	v_add_f32_e32 v4, v1, v39
	ds_write2_b32 v105, v1, v4 offset0:76 offset1:144
	v_add_f32_e32 v1, v4, v40
	v_add_f32_e32 v4, v1, v41
	ds_write2_b32 v106, v1, v4 offset0:84 offset1:152
	v_add_f32_e32 v1, v4, v42
	v_add_f32_e32 v4, v1, v43
	ds_write2_b32 v107, v1, v4 offset0:92 offset1:160
	v_add_f32_e32 v1, v4, v44
	v_add_f32_e32 v4, v1, v45
	ds_write2_b32 v108, v1, v4 offset0:100 offset1:168
	v_add_f32_e32 v1, v4, v46
	v_add_f32_e32 v4, v1, v47
	ds_write2_b32 v109, v1, v4 offset0:108 offset1:176
	v_add_f32_e32 v1, v4, v48
	v_add_f32_e32 v4, v1, v49
	ds_write2_b32 v110, v1, v4 offset0:116 offset1:184
	v_add_f32_e32 v1, v4, v50
	v_add_f32_e32 v4, v1, v51
	ds_write2_b32 v111, v1, v4 offset0:124 offset1:192
	v_add_f32_e32 v1, v4, v52
	v_add_f32_e32 v4, v1, v53
	ds_write2_b32 v112, v1, v4 offset0:4 offset1:72
	v_add_f32_e32 v1, v4, v54
	v_add_f32_e32 v4, v1, v55
	ds_write2_b32 v112, v1, v4 offset0:140 offset1:208
	v_add_f32_e32 v1, v4, v56
	v_add_f32_e32 v4, v1, v57
	ds_write2_b32 v113, v1, v4 offset0:20 offset1:88
	v_add_f32_e32 v1, v4, v58
	v_add_f32_e32 v4, v1, v59
	ds_write2_b32 v113, v1, v4 offset0:156 offset1:224
	v_add_f32_e32 v1, v4, v60
	v_add_f32_e32 v4, v1, v61
	ds_write2_b32 v114, v1, v4 offset0:36 offset1:104
	v_add_f32_e32 v1, v4, v62
	v_add_f32_e32 v4, v1, v63
	ds_write2_b32 v114, v1, v4 offset0:172 offset1:240
	v_add_f32_e32 v1, v4, v64
	v_add_f32_e32 v4, v1, v65
	ds_write2_b32 v115, v1, v4 offset0:52 offset1:120
	v_add_f32_e32 v1, v4, v66
	v_add_f32_e32 v4, v1, v67
	ds_write2_b32 v116, v1, v4 offset0:60 offset1:128
	v_or_b32_e32 v1, s5, v93
	v_add_u32_e32 v4, s8, v1
	v_sub_u32_e32 v1, v87, v86
	v_mov_b32_e32 v25, 0x1ff
	v_mov_b32_e32 v26, 0x200
	v_cvt_f32_i32_e32 v1, v1
	v_med3_i32 v5, v86, 0, v25
	v_med3_i32 v10, v87, 1, v26
	v_mad_u32_u24 v5, v5, s4, v0
	v_mad_u32_u24 v18, v10, s4, v0
	s_waitcnt lgkmcnt(0)
	s_barrier
	ds_read_b128 v[6:9], v5
	ds_read_b128 v[10:13], v18
	ds_read_b128 v[14:17], v5 offset:16
	ds_read_b128 v[18:21], v18 offset:16
	v_rcp_iflag_f32_e32 v22, v1
	s_mov_b64 s[0:1], 0x1000000
	v_ashrrev_i32_e32 v5, 31, v4
	s_waitcnt lgkmcnt(2)
	v_sub_f32_e32 v7, v11, v7
	v_sub_f32_e32 v6, v10, v6
	v_sub_f32_e32 v9, v13, v9
	v_sub_f32_e32 v8, v12, v8
	v_pk_mul_f32 v[10:11], v[8:9], v[22:23] op_sel_hi:[1,0]
	v_pk_mul_f32 v[12:13], v[6:7], v[22:23] op_sel_hi:[1,0]
	s_waitcnt lgkmcnt(0)
	v_sub_f32_e32 v7, v19, v15
	v_sub_f32_e32 v6, v18, v14
	v_sub_f32_e32 v9, v21, v17
	v_sub_f32_e32 v8, v20, v16
	v_pk_mul_f32 v[8:9], v[8:9], v[22:23] op_sel_hi:[1,0]
	v_pk_mul_f32 v[6:7], v[6:7], v[22:23] op_sel_hi:[1,0]
	v_lshl_add_u64 v[2:3], v[2:3], 0, s[0:1]
	v_cvt_pk_f16_f32 v9, v8, v9
	v_cvt_pk_f16_f32 v8, v6, v7
	v_cvt_pk_f16_f32 v7, v10, v11
	v_lshlrev_b64 v[10:11], 10, v[4:5]
	v_cvt_pk_f16_f32 v6, v12, v13
	v_lshl_add_u64 v[10:11], v[2:3], 0, v[10:11]
	v_sub_u32_e32 v1, v85, v84
	global_store_dwordx4 v[10:11], v[6:9], off nt
	v_cvt_f32_i32_e32 v1, v1
	v_med3_i32 v5, v84, 0, v25
	v_med3_i32 v10, v85, 1, v26
	v_mad_u32_u24 v5, v5, s4, v0
	v_mad_u32_u24 v18, v10, s4, v0
	ds_read_b128 v[6:9], v5
	ds_read_b128 v[10:13], v18
	ds_read_b128 v[14:17], v5 offset:16
	ds_read_b128 v[18:21], v18 offset:16
	v_rcp_iflag_f32_e32 v24, v1
	v_or_b32_e32 v22, 8, v4
	v_ashrrev_i32_e32 v23, 31, v22
	s_waitcnt lgkmcnt(2)
	v_sub_f32_e32 v7, v11, v7
	v_sub_f32_e32 v6, v10, v6
	v_sub_f32_e32 v9, v13, v9
	v_sub_f32_e32 v8, v12, v8
	v_pk_mul_f32 v[10:11], v[8:9], v[24:25] op_sel_hi:[1,0]
	v_pk_mul_f32 v[12:13], v[6:7], v[24:25] op_sel_hi:[1,0]
	s_waitcnt lgkmcnt(0)
	v_sub_f32_e32 v7, v19, v15
	v_sub_f32_e32 v6, v18, v14
	v_sub_f32_e32 v9, v21, v17
	v_sub_f32_e32 v8, v20, v16
	v_pk_mul_f32 v[8:9], v[8:9], v[24:25] op_sel_hi:[1,0]
	v_pk_mul_f32 v[6:7], v[6:7], v[24:25] op_sel_hi:[1,0]
	v_cvt_pk_f16_f32 v9, v8, v9
	v_cvt_pk_f16_f32 v8, v6, v7
	v_cvt_pk_f16_f32 v7, v10, v11
	v_lshlrev_b64 v[10:11], 10, v[22:23]
	v_cvt_pk_f16_f32 v6, v12, v13
	v_lshl_add_u64 v[10:11], v[2:3], 0, v[10:11]
	v_sub_u32_e32 v1, v83, v82
	global_store_dwordx4 v[10:11], v[6:9], off nt
	v_cvt_f32_i32_e32 v1, v1
	v_med3_i32 v5, v82, 0, v25
	v_med3_i32 v10, v83, 1, v26
	v_mad_u32_u24 v5, v5, s4, v0
	v_mad_u32_u24 v18, v10, s4, v0
	ds_read_b128 v[6:9], v5
	ds_read_b128 v[10:13], v18
	ds_read_b128 v[14:17], v5 offset:16
	ds_read_b128 v[18:21], v18 offset:16
	v_rcp_iflag_f32_e32 v24, v1
	v_or_b32_e32 v22, 16, v4
	v_ashrrev_i32_e32 v23, 31, v22
	s_waitcnt lgkmcnt(2)
	v_sub_f32_e32 v7, v11, v7
	v_sub_f32_e32 v6, v10, v6
	v_sub_f32_e32 v9, v13, v9
	v_sub_f32_e32 v8, v12, v8
	v_pk_mul_f32 v[10:11], v[8:9], v[24:25] op_sel_hi:[1,0]
	v_pk_mul_f32 v[12:13], v[6:7], v[24:25] op_sel_hi:[1,0]
	s_waitcnt lgkmcnt(0)
	v_sub_f32_e32 v7, v19, v15
	v_sub_f32_e32 v6, v18, v14
	v_sub_f32_e32 v9, v21, v17
	v_sub_f32_e32 v8, v20, v16
	v_pk_mul_f32 v[8:9], v[8:9], v[24:25] op_sel_hi:[1,0]
	v_pk_mul_f32 v[6:7], v[6:7], v[24:25] op_sel_hi:[1,0]
	v_cvt_pk_f16_f32 v9, v8, v9
	v_cvt_pk_f16_f32 v8, v6, v7
	v_cvt_pk_f16_f32 v7, v10, v11
	v_lshlrev_b64 v[10:11], 10, v[22:23]
	v_cvt_pk_f16_f32 v6, v12, v13
	v_lshl_add_u64 v[10:11], v[2:3], 0, v[10:11]
	v_sub_u32_e32 v1, v81, v80
	global_store_dwordx4 v[10:11], v[6:9], off nt
	v_cvt_f32_i32_e32 v1, v1
	v_med3_i32 v5, v80, 0, v25
	v_med3_i32 v10, v81, 1, v26
	v_mad_u32_u24 v5, v5, s4, v0
	v_mad_u32_u24 v18, v10, s4, v0
	ds_read_b128 v[6:9], v5
	ds_read_b128 v[10:13], v18
	ds_read_b128 v[14:17], v5 offset:16
	ds_read_b128 v[18:21], v18 offset:16
	v_rcp_iflag_f32_e32 v24, v1
	v_or_b32_e32 v22, 24, v4
	v_ashrrev_i32_e32 v23, 31, v22
	s_waitcnt lgkmcnt(2)
	v_sub_f32_e32 v7, v11, v7
	v_sub_f32_e32 v6, v10, v6
	v_sub_f32_e32 v9, v13, v9
	v_sub_f32_e32 v8, v12, v8
	v_pk_mul_f32 v[10:11], v[8:9], v[24:25] op_sel_hi:[1,0]
	v_pk_mul_f32 v[12:13], v[6:7], v[24:25] op_sel_hi:[1,0]
	s_waitcnt lgkmcnt(0)
	v_sub_f32_e32 v7, v19, v15
	v_sub_f32_e32 v6, v18, v14
	v_sub_f32_e32 v9, v21, v17
	v_sub_f32_e32 v8, v20, v16
	v_pk_mul_f32 v[8:9], v[8:9], v[24:25] op_sel_hi:[1,0]
	v_pk_mul_f32 v[6:7], v[6:7], v[24:25] op_sel_hi:[1,0]
	v_cvt_pk_f16_f32 v9, v8, v9
	v_cvt_pk_f16_f32 v8, v6, v7
	v_cvt_pk_f16_f32 v7, v10, v11
	v_lshlrev_b64 v[10:11], 10, v[22:23]
	v_cvt_pk_f16_f32 v6, v12, v13
	v_lshl_add_u64 v[10:11], v[2:3], 0, v[10:11]
	v_sub_u32_e32 v1, v79, v78
	global_store_dwordx4 v[10:11], v[6:9], off nt
	v_cvt_f32_i32_e32 v1, v1
	v_med3_i32 v5, v78, 0, v25
	v_med3_i32 v10, v79, 1, v26
	v_mad_u32_u24 v5, v5, s4, v0
	v_mad_u32_u24 v18, v10, s4, v0
	ds_read_b128 v[6:9], v5
	ds_read_b128 v[10:13], v18
	ds_read_b128 v[14:17], v5 offset:16
	ds_read_b128 v[18:21], v18 offset:16
	v_rcp_iflag_f32_e32 v24, v1
	v_or_b32_e32 v22, 32, v4
	v_ashrrev_i32_e32 v23, 31, v22
	s_waitcnt lgkmcnt(2)
	v_sub_f32_e32 v7, v11, v7
	v_sub_f32_e32 v6, v10, v6
	v_sub_f32_e32 v9, v13, v9
	v_sub_f32_e32 v8, v12, v8
	v_pk_mul_f32 v[10:11], v[8:9], v[24:25] op_sel_hi:[1,0]
	v_pk_mul_f32 v[12:13], v[6:7], v[24:25] op_sel_hi:[1,0]
	s_waitcnt lgkmcnt(0)
	v_sub_f32_e32 v7, v19, v15
	v_sub_f32_e32 v6, v18, v14
	v_sub_f32_e32 v9, v21, v17
	v_sub_f32_e32 v8, v20, v16
	v_pk_mul_f32 v[8:9], v[8:9], v[24:25] op_sel_hi:[1,0]
	v_pk_mul_f32 v[6:7], v[6:7], v[24:25] op_sel_hi:[1,0]
	v_cvt_pk_f16_f32 v9, v8, v9
	v_cvt_pk_f16_f32 v8, v6, v7
	v_cvt_pk_f16_f32 v7, v10, v11
	v_lshlrev_b64 v[10:11], 10, v[22:23]
	v_cvt_pk_f16_f32 v6, v12, v13
	v_lshl_add_u64 v[10:11], v[2:3], 0, v[10:11]
	v_sub_u32_e32 v1, v77, v76
	global_store_dwordx4 v[10:11], v[6:9], off nt
	v_cvt_f32_i32_e32 v1, v1
	v_med3_i32 v5, v76, 0, v25
	v_med3_i32 v10, v77, 1, v26
	v_mad_u32_u24 v5, v5, s4, v0
	v_mad_u32_u24 v18, v10, s4, v0
	ds_read_b128 v[6:9], v5
	ds_read_b128 v[10:13], v18
	ds_read_b128 v[14:17], v5 offset:16
	ds_read_b128 v[18:21], v18 offset:16
	v_rcp_iflag_f32_e32 v24, v1
	v_or_b32_e32 v22, 40, v4
	v_ashrrev_i32_e32 v23, 31, v22
	s_waitcnt lgkmcnt(2)
	v_sub_f32_e32 v7, v11, v7
	v_sub_f32_e32 v6, v10, v6
	v_sub_f32_e32 v9, v13, v9
	v_sub_f32_e32 v8, v12, v8
	v_pk_mul_f32 v[10:11], v[8:9], v[24:25] op_sel_hi:[1,0]
	v_pk_mul_f32 v[12:13], v[6:7], v[24:25] op_sel_hi:[1,0]
	s_waitcnt lgkmcnt(0)
	v_sub_f32_e32 v7, v19, v15
	v_sub_f32_e32 v6, v18, v14
	v_sub_f32_e32 v9, v21, v17
	v_sub_f32_e32 v8, v20, v16
	v_pk_mul_f32 v[8:9], v[8:9], v[24:25] op_sel_hi:[1,0]
	v_pk_mul_f32 v[6:7], v[6:7], v[24:25] op_sel_hi:[1,0]
	v_cvt_pk_f16_f32 v9, v8, v9
	v_cvt_pk_f16_f32 v8, v6, v7
	v_cvt_pk_f16_f32 v7, v10, v11
	v_lshlrev_b64 v[10:11], 10, v[22:23]
	v_cvt_pk_f16_f32 v6, v12, v13
	v_lshl_add_u64 v[10:11], v[2:3], 0, v[10:11]
	v_sub_u32_e32 v1, v75, v74
	global_store_dwordx4 v[10:11], v[6:9], off nt
	v_cvt_f32_i32_e32 v1, v1
	v_med3_i32 v5, v74, 0, v25
	v_med3_i32 v10, v75, 1, v26
	v_mad_u32_u24 v5, v5, s4, v0
	v_mad_u32_u24 v18, v10, s4, v0
	ds_read_b128 v[6:9], v5
	ds_read_b128 v[10:13], v18
	ds_read_b128 v[14:17], v5 offset:16
	ds_read_b128 v[18:21], v18 offset:16
	v_rcp_iflag_f32_e32 v24, v1
	v_or_b32_e32 v22, 48, v4
	v_ashrrev_i32_e32 v23, 31, v22
	s_waitcnt lgkmcnt(2)
	v_sub_f32_e32 v7, v11, v7
	v_sub_f32_e32 v6, v10, v6
	v_sub_f32_e32 v9, v13, v9
	v_sub_f32_e32 v8, v12, v8
	v_pk_mul_f32 v[10:11], v[8:9], v[24:25] op_sel_hi:[1,0]
	v_pk_mul_f32 v[12:13], v[6:7], v[24:25] op_sel_hi:[1,0]
	s_waitcnt lgkmcnt(0)
	v_sub_f32_e32 v7, v19, v15
	v_sub_f32_e32 v6, v18, v14
	v_sub_f32_e32 v9, v21, v17
	v_sub_f32_e32 v8, v20, v16
	v_pk_mul_f32 v[8:9], v[8:9], v[24:25] op_sel_hi:[1,0]
	v_pk_mul_f32 v[6:7], v[6:7], v[24:25] op_sel_hi:[1,0]
	v_cvt_pk_f16_f32 v9, v8, v9
	v_cvt_pk_f16_f32 v8, v6, v7
	v_cvt_pk_f16_f32 v7, v10, v11
	v_lshlrev_b64 v[10:11], 10, v[22:23]
	v_cvt_pk_f16_f32 v6, v12, v13
	v_lshl_add_u64 v[10:11], v[2:3], 0, v[10:11]
	v_sub_u32_e32 v1, v73, v72
	global_store_dwordx4 v[10:11], v[6:9], off nt
	v_cvt_f32_i32_e32 v1, v1
	v_med3_i32 v5, v72, 0, v25
	v_med3_i32 v10, v73, 1, v26
	v_mad_u32_u24 v5, v5, s4, v0
	v_mad_u32_u24 v18, v10, s4, v0
	ds_read_b128 v[6:9], v5
	ds_read_b128 v[10:13], v18
	ds_read_b128 v[14:17], v5 offset:16
	ds_read_b128 v[18:21], v18 offset:16
	v_or_b32_e32 v0, 56, v4
	v_rcp_iflag_f32_e32 v4, v1
	v_ashrrev_i32_e32 v1, 31, v0
	s_waitcnt lgkmcnt(2)
	v_sub_f32_e32 v7, v11, v7
	v_sub_f32_e32 v6, v10, v6
	v_sub_f32_e32 v9, v13, v9
	v_sub_f32_e32 v8, v12, v8
	v_pk_mul_f32 v[10:11], v[6:7], v[4:5] op_sel_hi:[1,0]
	s_waitcnt lgkmcnt(0)
	v_sub_f32_e32 v7, v19, v15
	v_sub_f32_e32 v6, v18, v14
	v_sub_f32_e32 v13, v21, v17
	v_sub_f32_e32 v12, v20, v16
	v_pk_mul_f32 v[8:9], v[8:9], v[4:5] op_sel_hi:[1,0]
	v_pk_mul_f32 v[12:13], v[12:13], v[4:5] op_sel_hi:[1,0]
	v_pk_mul_f32 v[4:5], v[6:7], v[4:5] op_sel_hi:[1,0]
	v_lshlrev_b64 v[0:1], 10, v[0:1]
	v_cvt_pk_f16_f32 v7, v12, v13
	v_cvt_pk_f16_f32 v6, v4, v5
	v_cvt_pk_f16_f32 v5, v8, v9
	v_cvt_pk_f16_f32 v4, v10, v11
	v_lshl_add_u64 v[0:1], v[2:3], 0, v[0:1]
	global_store_dwordx4 v[0:1], v[4:7], off nt
	s_endpgm
	.p2align	8

_ZN12_GLOBAL__N_14k_fcEPKtPKiS1_PKfS5_Pf:
	s_load_dwordx8 s[4:11], s[0:1], 0x0
	s_load_dwordx4 s[12:15], s[0:1], 0x20
	s_and_b32 s3, s2, 7
	s_lshr_b32 s20, s2, 3
	s_lshr_b32 s19, s20, 2
	s_lshl_b32 s3, s3, 3
	s_add_u32 s19, s19, s3
	s_and_b32 s20, s20, 3
	v_lshrrev_b32_e32 v1, 6, v0
	v_and_b32_e32 v12, 63, v0
	v_and_b32_e32 v13, 15, v0
	v_readfirstlane_b32 s16, v1
	v_lshrrev_b32_e32 v14, 4, v12
	s_nop 3
	s_lshr_b32 s17, s16, 2
	s_and_b32 s18, s16, 3
	v_lshlrev_b32_e32 v15, 6, v13
	v_lshl_add_u32 v15, v14, 4, v15
	v_lshrrev_b32_e32 v56, 3, v13
	v_lshlrev_b32_e32 v56, 5, v56
	v_xor_b32_e32 v15, v15, v56
	s_lshl_b32 s42, s17, 13
	v_add_u32_e32 v1, s42, v15
	v_add_u32_e32 v2, 0x14000, v1
	s_mul_i32 s42, s18, 0x1800
	s_add_u32 s42, s42, 0x4000
	v_add_u32_e32 v3, s42, v15
	v_add_u32_e32 v4, 0x14000, v3
	v_lshrrev_b32_e32 v57, 2, v12
	v_and_b32_e32 v58, 3, v12
	v_lshrrev_b32_e32 v59, 5, v12
	v_lshlrev_b32_e32 v59, 1, v59
	v_xor_b32_e32 v58, v58, v59
	v_lshlrev_b32_e32 v58, 4, v58
	s_lshl_b32 s42, s19, 8
	s_lshl_b32 s43, s16, 5
	s_add_u32 s42, s42, s43
	v_add_u32_e32 v60, s42, v57
	v_add_u32_e32 v61, 16, v60
	v_lshlrev_b32_e32 v62, 3, v60
	v_lshlrev_b32_e32 v63, 3, v61
	s_waitcnt lgkmcnt(0)
	global_load_dwordx2 v[40:41], v62, s[6:7]
	global_load_dwordx2 v[42:43], v63, s[6:7]
	v_mul_u32_u24_e32 v11, 0xc00, v57
	v_add_u32_e32 v11, v11, v58
	s_mul_i32 s42, s20, 0x180
	s_mul_i32 s43, s16, 48
	s_add_u32 s42, s42, s43
	s_mul_i32 s42, s42, 0xc00
	s_add_u32 s28, s8, s42
	s_addc_u32 s29, s9, 0
	s_add_u32 s30, s28, 64
	s_addc_u32 s31, s29, 0
	s_add_u32 s32, s28, 0xc000
	s_addc_u32 s33, s29, 0
	s_add_u32 s34, s32, 64
	s_addc_u32 s35, s33, 0
	s_add_u32 s36, s28, 0x18000
	s_addc_u32 s37, s29, 0
	s_add_u32 s38, s36, 64
	s_addc_u32 s39, s37, 0
	s_mov_b64 s[24:25], s[4:5]
	s_add_u32 s26, s4, 64
	s_addc_u32 s27, s5, 0
	s_add_u32 s40, s4, 0x1000000
	s_addc_u32 s41, s5, 0
	s_lshl_b32 s22, s16, 11
	s_mul_i32 s23, s16, 0xc00
	s_add_u32 s23, s23, 0x4000
	s_mov_b32 s21, 0
	s_lshr_b32 s44, s19, 1
	s_lshl_b32 s44, s44, 9
	s_movk_i32 s45, 0x1ff
	s_movk_i32 s46, 0x200
	v_mov_b32_e32 v64, 0
	v_mov_b32_e32 v65, 0
	v_mov_b32_e32 v66, 0
	v_mov_b32_e32 v67, 0
	v_mov_b32_e32 v68, 0
	v_mov_b32_e32 v69, 0
	v_mov_b32_e32 v70, 0
	v_mov_b32_e32 v71, 0
	v_mov_b32_e32 v72, 0
	v_mov_b32_e32 v73, 0
	v_mov_b32_e32 v74, 0
	v_mov_b32_e32 v75, 0
	v_mov_b32_e32 v76, 0
	v_mov_b32_e32 v77, 0
	v_mov_b32_e32 v78, 0
	v_mov_b32_e32 v79, 0
	v_mov_b32_e32 v80, 0
	v_mov_b32_e32 v81, 0
	v_mov_b32_e32 v82, 0
	v_mov_b32_e32 v83, 0
	v_mov_b32_e32 v84, 0
	v_mov_b32_e32 v85, 0
	v_mov_b32_e32 v86, 0
	v_mov_b32_e32 v87, 0
	v_mov_b32_e32 v88, 0
	v_mov_b32_e32 v89, 0
	v_mov_b32_e32 v90, 0
	v_mov_b32_e32 v91, 0
	v_mov_b32_e32 v92, 0
	v_mov_b32_e32 v93, 0
	v_mov_b32_e32 v94, 0
	v_mov_b32_e32 v95, 0
	v_mov_b32_e32 v96, 0
	v_mov_b32_e32 v97, 0
	v_mov_b32_e32 v98, 0
	v_mov_b32_e32 v99, 0
	v_mov_b32_e32 v100, 0
	v_mov_b32_e32 v101, 0
	v_mov_b32_e32 v102, 0
	v_mov_b32_e32 v103, 0
	v_mov_b32_e32 v104, 0
	v_mov_b32_e32 v105, 0
	v_mov_b32_e32 v106, 0
	v_mov_b32_e32 v107, 0
	v_mov_b32_e32 v108, 0
	v_mov_b32_e32 v109, 0
	v_mov_b32_e32 v110, 0
	v_mov_b32_e32 v111, 0
	v_mov_b32_e32 v112, 0
	v_mov_b32_e32 v113, 0
	v_mov_b32_e32 v114, 0
	v_mov_b32_e32 v115, 0
	v_mov_b32_e32 v116, 0
	v_mov_b32_e32 v117, 0
	v_mov_b32_e32 v118, 0
	v_mov_b32_e32 v119, 0
	v_mov_b32_e32 v120, 0
	v_mov_b32_e32 v121, 0
	v_mov_b32_e32 v122, 0
	v_mov_b32_e32 v123, 0
	v_mov_b32_e32 v124, 0
	v_mov_b32_e32 v125, 0
	v_mov_b32_e32 v126, 0
	v_mov_b32_e32 v127, 0
	v_mov_b32_e32 v128, 0
	v_mov_b32_e32 v129, 0
	v_mov_b32_e32 v130, 0
	v_mov_b32_e32 v131, 0
	v_mov_b32_e32 v132, 0
	v_mov_b32_e32 v133, 0
	v_mov_b32_e32 v134, 0
	v_mov_b32_e32 v135, 0
	v_mov_b32_e32 v136, 0
	v_mov_b32_e32 v137, 0
	v_mov_b32_e32 v138, 0
	v_mov_b32_e32 v139, 0
	v_mov_b32_e32 v140, 0
	v_mov_b32_e32 v141, 0
	v_mov_b32_e32 v142, 0
	v_mov_b32_e32 v143, 0
	v_mov_b32_e32 v144, 0
	v_mov_b32_e32 v145, 0
	v_mov_b32_e32 v146, 0
	v_mov_b32_e32 v147, 0
	v_mov_b32_e32 v148, 0
	v_mov_b32_e32 v149, 0
	v_mov_b32_e32 v150, 0
	v_mov_b32_e32 v151, 0
	v_mov_b32_e32 v152, 0
	v_mov_b32_e32 v153, 0
	v_mov_b32_e32 v154, 0
	v_mov_b32_e32 v155, 0
	v_mov_b32_e32 v156, 0
	v_mov_b32_e32 v157, 0
	v_mov_b32_e32 v158, 0
	v_mov_b32_e32 v159, 0
	v_mov_b32_e32 v160, 0
	v_mov_b32_e32 v161, 0
	v_mov_b32_e32 v162, 0
	v_mov_b32_e32 v163, 0
	v_mov_b32_e32 v164, 0
	v_mov_b32_e32 v165, 0
	v_mov_b32_e32 v166, 0
	v_mov_b32_e32 v167, 0
	v_mov_b32_e32 v168, 0
	v_mov_b32_e32 v169, 0
	v_mov_b32_e32 v170, 0
	v_mov_b32_e32 v171, 0
	v_mov_b32_e32 v172, 0
	v_mov_b32_e32 v173, 0
	v_mov_b32_e32 v174, 0
	v_mov_b32_e32 v175, 0
	v_mov_b32_e32 v176, 0
	v_mov_b32_e32 v177, 0
	v_mov_b32_e32 v178, 0
	v_mov_b32_e32 v179, 0
	v_mov_b32_e32 v180, 0
	v_mov_b32_e32 v181, 0
	v_mov_b32_e32 v182, 0
	v_mov_b32_e32 v183, 0
	v_mov_b32_e32 v184, 0
	v_mov_b32_e32 v185, 0
	v_mov_b32_e32 v186, 0
	v_mov_b32_e32 v187, 0
	v_mov_b32_e32 v188, 0
	v_mov_b32_e32 v189, 0
	v_mov_b32_e32 v190, 0
	v_mov_b32_e32 v191, 0
	v_mov_b32_e32 v192, 0
	v_mov_b32_e32 v193, 0
	v_mov_b32_e32 v194, 0
	v_mov_b32_e32 v195, 0
	v_mov_b32_e32 v196, 0
	v_mov_b32_e32 v197, 0
	v_mov_b32_e32 v198, 0
	v_mov_b32_e32 v199, 0
	v_mov_b32_e32 v200, 0
	v_mov_b32_e32 v201, 0
	v_mov_b32_e32 v202, 0
	v_mov_b32_e32 v203, 0
	v_mov_b32_e32 v204, 0
	v_mov_b32_e32 v205, 0
	v_mov_b32_e32 v206, 0
	v_mov_b32_e32 v207, 0
	v_mov_b32_e32 v208, 0
	v_mov_b32_e32 v209, 0
	v_mov_b32_e32 v210, 0
	v_mov_b32_e32 v211, 0
	v_mov_b32_e32 v212, 0
	v_mov_b32_e32 v213, 0
	v_mov_b32_e32 v214, 0
	v_mov_b32_e32 v215, 0
	v_mov_b32_e32 v216, 0
	v_mov_b32_e32 v217, 0
	v_mov_b32_e32 v218, 0
	v_mov_b32_e32 v219, 0
	v_mov_b32_e32 v220, 0
	v_mov_b32_e32 v221, 0
	v_mov_b32_e32 v222, 0
	v_mov_b32_e32 v223, 0
	v_mov_b32_e32 v224, 0
	v_mov_b32_e32 v225, 0
	v_mov_b32_e32 v226, 0
	v_mov_b32_e32 v227, 0
	v_mov_b32_e32 v228, 0
	v_mov_b32_e32 v229, 0
	v_mov_b32_e32 v230, 0
	v_mov_b32_e32 v231, 0
	v_mov_b32_e32 v232, 0
	v_mov_b32_e32 v233, 0
	v_mov_b32_e32 v234, 0
	v_mov_b32_e32 v235, 0
	v_mov_b32_e32 v236, 0
	v_mov_b32_e32 v237, 0
	v_mov_b32_e32 v238, 0
	v_mov_b32_e32 v239, 0
	v_mov_b32_e32 v240, 0
	v_mov_b32_e32 v241, 0
	v_mov_b32_e32 v242, 0
	v_mov_b32_e32 v243, 0
	v_mov_b32_e32 v244, 0
	v_mov_b32_e32 v245, 0
	v_mov_b32_e32 v246, 0
	v_mov_b32_e32 v247, 0
	v_mov_b32_e32 v248, 0
	v_mov_b32_e32 v249, 0
	v_mov_b32_e32 v250, 0
	v_mov_b32_e32 v251, 0
	v_mov_b32_e32 v252, 0
	v_mov_b32_e32 v253, 0
	v_mov_b32_e32 v254, 0
	v_mov_b32_e32 v255, 0
	s_waitcnt vmcnt(0)
	v_med3_i32 v40, v40, 0, s45
	v_med3_i32 v41, v41, 1, s46
	v_med3_i32 v42, v42, 0, s45
	v_med3_i32 v43, v43, 1, s46
	v_add_u32_e32 v40, s44, v40
	v_add_u32_e32 v42, s44, v42
	v_add_u32_e32 v41, s44, v41
	v_add_u32_e32 v43, s44, v43
	v_add_u32_e32 v41, -1, v41
	v_add_u32_e32 v43, -1, v43
	v_lshl_add_u32 v5, v40, 10, v58
	v_lshl_add_u32 v6, v42, 10, v58
	v_lshl_add_u32 v7, v60, 10, v58
	v_lshl_add_u32 v8, v61, 10, v58
	v_lshl_add_u32 v9, v41, 10, v58
	v_lshl_add_u32 v10, v43, 10, v58
	s_add_u32 m0, s22, 0x0
	s_nop 0
	global_load_lds_dwordx4 v5, s[24:25]
	s_add_u32 m0, s22, 0xa000
	s_nop 0
	global_load_lds_dwordx4 v5, s[26:27]
	s_add_u32 m0, s22, 0x400
	s_nop 0
	global_load_lds_dwordx4 v6, s[24:25]
	s_add_u32 m0, s22, 0xa400
	s_nop 0
	global_load_lds_dwordx4 v6, s[26:27]
	s_add_u32 m0, s23, 0x0
	s_nop 0
	global_load_lds_dwordx4 v11, s[28:29]
	s_add_u32 m0, s23, 0xa000
	s_nop 0
	global_load_lds_dwordx4 v11, s[30:31]
	s_add_u32 m0, s23, 0x400
	s_nop 0
	global_load_lds_dwordx4 v11, s[32:33]
	s_add_u32 m0, s23, 0xa400
	s_nop 0
	global_load_lds_dwordx4 v11, s[34:35]
	s_add_u32 m0, s23, 0x800
	s_nop 0
	global_load_lds_dwordx4 v11, s[36:37]
	s_add_u32 m0, s23, 0xa800
	s_nop 0
	global_load_lds_dwordx4 v11, s[38:39]
	s_add_u32 s24, s24, 0x80
	s_addc_u32 s25, s25, 0
	s_add_u32 s26, s26, 0x80
	s_addc_u32 s27, s27, 0
	s_add_u32 s28, s28, 0x80
	s_addc_u32 s29, s29, 0
	s_add_u32 s30, s30, 0x80
	s_addc_u32 s31, s31, 0
	s_add_u32 s32, s32, 0x80
	s_addc_u32 s33, s33, 0
	s_add_u32 s34, s34, 0x80
	s_addc_u32 s35, s35, 0
	s_add_u32 s36, s36, 0x80
	s_addc_u32 s37, s37, 0
	s_add_u32 s38, s38, 0x80
	s_addc_u32 s39, s39, 0
	s_waitcnt vmcnt(0)
	s_barrier
	s_cmp_lg_u32 s17, 0
	s_cbranch_scc1 .Lfc_h1_entry
.Lfc_h0_loop:
	ds_read_b128 v[16:19], v3 offset:0
	ds_read_b128 v[20:23], v3 offset:1024
	ds_read_b128 v[24:27], v3 offset:2048
	ds_read_b128 v[28:31], v3 offset:3072
	ds_read_b128 v[32:35], v3 offset:4096
	ds_read_b128 v[36:39], v3 offset:5120
	ds_read_b128 v[40:43], v1 offset:0
	ds_read_b128 v[44:47], v1 offset:1024
	ds_read_b128 v[48:51], v1 offset:2048
	ds_read_b128 v[52:55], v1 offset:3072
	s_barrier
	s_waitcnt lgkmcnt(0)
	s_setprio 1
	v_mfma_f32_16x16x32_f16 v[64:67], v[16:19], v[40:43], v[64:67]
	v_mfma_f32_16x16x32_f16 v[68:71], v[20:23], v[40:43], v[68:71]
	v_mfma_f32_16x16x32_f16 v[72:75], v[24:27], v[40:43], v[72:75]
	v_mfma_f32_16x16x32_f16 v[76:79], v[28:31], v[40:43], v[76:79]
	v_mfma_f32_16x16x32_f16 v[80:83], v[32:35], v[40:43], v[80:83]
	v_mfma_f32_16x16x32_f16 v[84:87], v[36:39], v[40:43], v[84:87]
	v_mfma_f32_16x16x32_f16 v[88:91], v[16:19], v[44:47], v[88:91]
	ds_read_b128 v[40:43], v1 offset:4096
	v_mfma_f32_16x16x32_f16 v[92:95], v[20:23], v[44:47], v[92:95]
	v_mfma_f32_16x16x32_f16 v[96:99], v[24:27], v[44:47], v[96:99]
	v_mfma_f32_16x16x32_f16 v[100:103], v[28:31], v[44:47], v[100:103]
	v_mfma_f32_16x16x32_f16 v[104:107], v[32:35], v[44:47], v[104:107]
	v_mfma_f32_16x16x32_f16 v[108:111], v[36:39], v[44:47], v[108:111]
	v_mfma_f32_16x16x32_f16 v[112:115], v[16:19], v[48:51], v[112:115]
	ds_read_b128 v[44:47], v1 offset:5120
	v_mfma_f32_16x16x32_f16 v[116:119], v[20:23], v[48:51], v[116:119]
	v_mfma_f32_16x16x32_f16 v[120:123], v[24:27], v[48:51], v[120:123]
	v_mfma_f32_16x16x32_f16 v[124:127], v[28:31], v[48:51], v[124:127]
	v_mfma_f32_16x16x32_f16 v[128:131], v[32:35], v[48:51], v[128:131]
	v_mfma_f32_16x16x32_f16 v[132:135], v[36:39], v[48:51], v[132:135]
	v_mfma_f32_16x16x32_f16 v[136:139], v[16:19], v[52:55], v[136:139]
	ds_read_b128 v[48:51], v1 offset:6144
	v_mfma_f32_16x16x32_f16 v[140:143], v[20:23], v[52:55], v[140:143]
	v_mfma_f32_16x16x32_f16 v[144:147], v[24:27], v[52:55], v[144:147]
	v_mfma_f32_16x16x32_f16 v[148:151], v[28:31], v[52:55], v[148:151]
	v_mfma_f32_16x16x32_f16 v[152:155], v[32:35], v[52:55], v[152:155]
	v_mfma_f32_16x16x32_f16 v[156:159], v[36:39], v[52:55], v[156:159]
	s_waitcnt lgkmcnt(2)
	v_mfma_f32_16x16x32_f16 v[160:163], v[16:19], v[40:43], v[160:163]
	ds_read_b128 v[52:55], v1 offset:7168
	v_mfma_f32_16x16x32_f16 v[164:167], v[20:23], v[40:43], v[164:167]
	v_mfma_f32_16x16x32_f16 v[168:171], v[24:27], v[40:43], v[168:171]
	v_mfma_f32_16x16x32_f16 v[172:175], v[28:31], v[40:43], v[172:175]
	v_mfma_f32_16x16x32_f16 v[176:179], v[32:35], v[40:43], v[176:179]
	v_mfma_f32_16x16x32_f16 v[180:183], v[36:39], v[40:43], v[180:183]
	s_waitcnt lgkmcnt(2)
	v_mfma_f32_16x16x32_f16 v[184:187], v[16:19], v[44:47], v[184:187]
	v_mfma_f32_16x16x32_f16 v[188:191], v[20:23], v[44:47], v[188:191]
	v_mfma_f32_16x16x32_f16 v[192:195], v[24:27], v[44:47], v[192:195]
	v_mfma_f32_16x16x32_f16 v[196:199], v[28:31], v[44:47], v[196:199]
	v_mfma_f32_16x16x32_f16 v[200:203], v[32:35], v[44:47], v[200:203]
	v_mfma_f32_16x16x32_f16 v[204:207], v[36:39], v[44:47], v[204:207]
	s_waitcnt lgkmcnt(1)
	v_mfma_f32_16x16x32_f16 v[208:211], v[16:19], v[48:51], v[208:211]
	v_mfma_f32_16x16x32_f16 v[212:215], v[20:23], v[48:51], v[212:215]
	v_mfma_f32_16x16x32_f16 v[216:219], v[24:27], v[48:51], v[216:219]
	v_mfma_f32_16x16x32_f16 v[220:223], v[28:31], v[48:51], v[220:223]
	v_mfma_f32_16x16x32_f16 v[224:227], v[32:35], v[48:51], v[224:227]
	v_mfma_f32_16x16x32_f16 v[228:231], v[36:39], v[48:51], v[228:231]
	s_waitcnt lgkmcnt(0)
	v_mfma_f32_16x16x32_f16 v[232:235], v[16:19], v[52:55], v[232:235]
	v_mfma_f32_16x16x32_f16 v[236:239], v[20:23], v[52:55], v[236:239]
	v_mfma_f32_16x16x32_f16 v[240:243], v[24:27], v[52:55], v[240:243]
	v_mfma_f32_16x16x32_f16 v[244:247], v[28:31], v[52:55], v[244:247]
	v_mfma_f32_16x16x32_f16 v[248:251], v[32:35], v[52:55], v[248:251]
	v_mfma_f32_16x16x32_f16 v[252:255], v[36:39], v[52:55], v[252:255]
	s_setprio 0
	s_barrier
	ds_read_b128 v[16:19], v3 offset:40960
	ds_read_b128 v[20:23], v3 offset:41984
	ds_read_b128 v[24:27], v3 offset:43008
	ds_read_b128 v[28:31], v3 offset:44032
	ds_read_b128 v[32:35], v3 offset:45056
	ds_read_b128 v[36:39], v3 offset:46080
	ds_read_b128 v[40:43], v1 offset:40960
	ds_read_b128 v[44:47], v1 offset:41984
	ds_read_b128 v[48:51], v1 offset:43008
	ds_read_b128 v[52:55], v1 offset:44032
	s_add_u32 m0, s22, 0x14000
	s_nop 0
	global_load_lds_dwordx4 v5, s[24:25]
	s_add_u32 m0, s22, 0x1e000
	s_nop 0
	global_load_lds_dwordx4 v5, s[26:27]
	s_add_u32 m0, s22, 0x14400
	s_nop 0
	global_load_lds_dwordx4 v6, s[24:25]
	s_add_u32 m0, s22, 0x1e400
	s_nop 0
	global_load_lds_dwordx4 v6, s[26:27]
	s_add_u32 m0, s23, 0x14000
	s_nop 0
	global_load_lds_dwordx4 v11, s[28:29]
	s_add_u32 m0, s23, 0x1e000
	s_nop 0
	global_load_lds_dwordx4 v11, s[30:31]
	s_add_u32 m0, s23, 0x14400
	s_nop 0
	global_load_lds_dwordx4 v11, s[32:33]
	s_add_u32 m0, s23, 0x1e400
	s_nop 0
	global_load_lds_dwordx4 v11, s[34:35]
	s_add_u32 m0, s23, 0x14800
	s_nop 0
	global_load_lds_dwordx4 v11, s[36:37]
	s_add_u32 m0, s23, 0x1e800
	s_nop 0
	global_load_lds_dwordx4 v11, s[38:39]
	s_add_u32 s28, s28, 0x80
	s_addc_u32 s29, s29, 0
	s_add_u32 s30, s30, 0x80
	s_addc_u32 s31, s31, 0
	s_add_u32 s32, s32, 0x80
	s_addc_u32 s33, s33, 0
	s_add_u32 s34, s34, 0x80
	s_addc_u32 s35, s35, 0
	s_add_u32 s36, s36, 0x80
	s_addc_u32 s37, s37, 0
	s_add_u32 s38, s38, 0x80
	s_addc_u32 s39, s39, 0
	s_cmp_eq_u32 s21, 3
	s_cbranch_scc1 .Lfc_sw_h0
	s_cmp_eq_u32 s21, 7
	s_cbranch_scc1 .Lfc_sw_h0
	s_add_u32 s24, s24, 0x80
	s_addc_u32 s25, s25, 0
	s_add_u32 s26, s26, 0x80
	s_addc_u32 s27, s27, 0
	s_branch .Lfc_swd_h0
.Lfc_sw_h0:
	s_mov_b64 s[24:25], s[40:41]
	s_add_u32 s26, s40, 64
	s_addc_u32 s27, s41, 0
	s_mov_b64 s[40:41], s[4:5]
	v_mov_b32_e32 v5, v7
	v_mov_b32_e32 v6, v8
	v_mov_b32_e32 v7, v9
	v_mov_b32_e32 v8, v10
.Lfc_swd_h0:
	s_barrier
	s_waitcnt lgkmcnt(0)
	s_setprio 1
	v_mfma_f32_16x16x32_f16 v[64:67], v[16:19], v[40:43], v[64:67]
	v_mfma_f32_16x16x32_f16 v[68:71], v[20:23], v[40:43], v[68:71]
	v_mfma_f32_16x16x32_f16 v[72:75], v[24:27], v[40:43], v[72:75]
	v_mfma_f32_16x16x32_f16 v[76:79], v[28:31], v[40:43], v[76:79]
	v_mfma_f32_16x16x32_f16 v[80:83], v[32:35], v[40:43], v[80:83]
	v_mfma_f32_16x16x32_f16 v[84:87], v[36:39], v[40:43], v[84:87]
	v_mfma_f32_16x16x32_f16 v[88:91], v[16:19], v[44:47], v[88:91]
	ds_read_b128 v[40:43], v1 offset:45056
	v_mfma_f32_16x16x32_f16 v[92:95], v[20:23], v[44:47], v[92:95]
	v_mfma_f32_16x16x32_f16 v[96:99], v[24:27], v[44:47], v[96:99]
	v_mfma_f32_16x16x32_f16 v[100:103], v[28:31], v[44:47], v[100:103]
	v_mfma_f32_16x16x32_f16 v[104:107], v[32:35], v[44:47], v[104:107]
	v_mfma_f32_16x16x32_f16 v[108:111], v[36:39], v[44:47], v[108:111]
	v_mfma_f32_16x16x32_f16 v[112:115], v[16:19], v[48:51], v[112:115]
	ds_read_b128 v[44:47], v1 offset:46080
	v_mfma_f32_16x16x32_f16 v[116:119], v[20:23], v[48:51], v[116:119]
	v_mfma_f32_16x16x32_f16 v[120:123], v[24:27], v[48:51], v[120:123]
	v_mfma_f32_16x16x32_f16 v[124:127], v[28:31], v[48:51], v[124:127]
	v_mfma_f32_16x16x32_f16 v[128:131], v[32:35], v[48:51], v[128:131]
	v_mfma_f32_16x16x32_f16 v[132:135], v[36:39], v[48:51], v[132:135]
	v_mfma_f32_16x16x32_f16 v[136:139], v[16:19], v[52:55], v[136:139]
	ds_read_b128 v[48:51], v1 offset:47104
	v_mfma_f32_16x16x32_f16 v[140:143], v[20:23], v[52:55], v[140:143]
	v_mfma_f32_16x16x32_f16 v[144:147], v[24:27], v[52:55], v[144:147]
	v_mfma_f32_16x16x32_f16 v[148:151], v[28:31], v[52:55], v[148:151]
	v_mfma_f32_16x16x32_f16 v[152:155], v[32:35], v[52:55], v[152:155]
	v_mfma_f32_16x16x32_f16 v[156:159], v[36:39], v[52:55], v[156:159]
	s_waitcnt lgkmcnt(2)
	v_mfma_f32_16x16x32_f16 v[160:163], v[16:19], v[40:43], v[160:163]
	ds_read_b128 v[52:55], v1 offset:48128
	v_mfma_f32_16x16x32_f16 v[164:167], v[20:23], v[40:43], v[164:167]
	v_mfma_f32_16x16x32_f16 v[168:171], v[24:27], v[40:43], v[168:171]
	v_mfma_f32_16x16x32_f16 v[172:175], v[28:31], v[40:43], v[172:175]
	v_mfma_f32_16x16x32_f16 v[176:179], v[32:35], v[40:43], v[176:179]
	v_mfma_f32_16x16x32_f16 v[180:183], v[36:39], v[40:43], v[180:183]
	s_waitcnt lgkmcnt(2)
	v_mfma_f32_16x16x32_f16 v[184:187], v[16:19], v[44:47], v[184:187]
	v_mfma_f32_16x16x32_f16 v[188:191], v[20:23], v[44:47], v[188:191]
	v_mfma_f32_16x16x32_f16 v[192:195], v[24:27], v[44:47], v[192:195]
	v_mfma_f32_16x16x32_f16 v[196:199], v[28:31], v[44:47], v[196:199]
	v_mfma_f32_16x16x32_f16 v[200:203], v[32:35], v[44:47], v[200:203]
	v_mfma_f32_16x16x32_f16 v[204:207], v[36:39], v[44:47], v[204:207]
	s_waitcnt lgkmcnt(1)
	v_mfma_f32_16x16x32_f16 v[208:211], v[16:19], v[48:51], v[208:211]
	v_mfma_f32_16x16x32_f16 v[212:215], v[20:23], v[48:51], v[212:215]
	v_mfma_f32_16x16x32_f16 v[216:219], v[24:27], v[48:51], v[216:219]
	v_mfma_f32_16x16x32_f16 v[220:223], v[28:31], v[48:51], v[220:223]
	v_mfma_f32_16x16x32_f16 v[224:227], v[32:35], v[48:51], v[224:227]
	v_mfma_f32_16x16x32_f16 v[228:231], v[36:39], v[48:51], v[228:231]
	s_waitcnt lgkmcnt(0)
	v_mfma_f32_16x16x32_f16 v[232:235], v[16:19], v[52:55], v[232:235]
	v_mfma_f32_16x16x32_f16 v[236:239], v[20:23], v[52:55], v[236:239]
	v_mfma_f32_16x16x32_f16 v[240:243], v[24:27], v[52:55], v[240:243]
	v_mfma_f32_16x16x32_f16 v[244:247], v[28:31], v[52:55], v[244:247]
	v_mfma_f32_16x16x32_f16 v[248:251], v[32:35], v[52:55], v[248:251]
	v_mfma_f32_16x16x32_f16 v[252:255], v[36:39], v[52:55], v[252:255]
	s_setprio 0
	s_waitcnt vmcnt(0)
	s_barrier
	ds_read_b128 v[16:19], v4 offset:0
	ds_read_b128 v[20:23], v4 offset:1024
	ds_read_b128 v[24:27], v4 offset:2048
	ds_read_b128 v[28:31], v4 offset:3072
	ds_read_b128 v[32:35], v4 offset:4096
	ds_read_b128 v[36:39], v4 offset:5120
	ds_read_b128 v[40:43], v2 offset:0
	ds_read_b128 v[44:47], v2 offset:1024
	ds_read_b128 v[48:51], v2 offset:2048
	ds_read_b128 v[52:55], v2 offset:3072
	s_barrier
	s_waitcnt lgkmcnt(0)
	s_setprio 1
	v_mfma_f32_16x16x32_f16 v[64:67], v[16:19], v[40:43], v[64:67]
	v_mfma_f32_16x16x32_f16 v[68:71], v[20:23], v[40:43], v[68:71]
	v_mfma_f32_16x16x32_f16 v[72:75], v[24:27], v[40:43], v[72:75]
	v_mfma_f32_16x16x32_f16 v[76:79], v[28:31], v[40:43], v[76:79]
	v_mfma_f32_16x16x32_f16 v[80:83], v[32:35], v[40:43], v[80:83]
	v_mfma_f32_16x16x32_f16 v[84:87], v[36:39], v[40:43], v[84:87]
	v_mfma_f32_16x16x32_f16 v[88:91], v[16:19], v[44:47], v[88:91]
	ds_read_b128 v[40:43], v2 offset:4096
	v_mfma_f32_16x16x32_f16 v[92:95], v[20:23], v[44:47], v[92:95]
	v_mfma_f32_16x16x32_f16 v[96:99], v[24:27], v[44:47], v[96:99]
	v_mfma_f32_16x16x32_f16 v[100:103], v[28:31], v[44:47], v[100:103]
	v_mfma_f32_16x16x32_f16 v[104:107], v[32:35], v[44:47], v[104:107]
	v_mfma_f32_16x16x32_f16 v[108:111], v[36:39], v[44:47], v[108:111]
	v_mfma_f32_16x16x32_f16 v[112:115], v[16:19], v[48:51], v[112:115]
	ds_read_b128 v[44:47], v2 offset:5120
	v_mfma_f32_16x16x32_f16 v[116:119], v[20:23], v[48:51], v[116:119]
	v_mfma_f32_16x16x32_f16 v[120:123], v[24:27], v[48:51], v[120:123]
	v_mfma_f32_16x16x32_f16 v[124:127], v[28:31], v[48:51], v[124:127]
	v_mfma_f32_16x16x32_f16 v[128:131], v[32:35], v[48:51], v[128:131]
	v_mfma_f32_16x16x32_f16 v[132:135], v[36:39], v[48:51], v[132:135]
	v_mfma_f32_16x16x32_f16 v[136:139], v[16:19], v[52:55], v[136:139]
	ds_read_b128 v[48:51], v2 offset:6144
	v_mfma_f32_16x16x32_f16 v[140:143], v[20:23], v[52:55], v[140:143]
	v_mfma_f32_16x16x32_f16 v[144:147], v[24:27], v[52:55], v[144:147]
	v_mfma_f32_16x16x32_f16 v[148:151], v[28:31], v[52:55], v[148:151]
	v_mfma_f32_16x16x32_f16 v[152:155], v[32:35], v[52:55], v[152:155]
	v_mfma_f32_16x16x32_f16 v[156:159], v[36:39], v[52:55], v[156:159]
	s_waitcnt lgkmcnt(2)
	v_mfma_f32_16x16x32_f16 v[160:163], v[16:19], v[40:43], v[160:163]
	ds_read_b128 v[52:55], v2 offset:7168
	v_mfma_f32_16x16x32_f16 v[164:167], v[20:23], v[40:43], v[164:167]
	v_mfma_f32_16x16x32_f16 v[168:171], v[24:27], v[40:43], v[168:171]
	v_mfma_f32_16x16x32_f16 v[172:175], v[28:31], v[40:43], v[172:175]
	v_mfma_f32_16x16x32_f16 v[176:179], v[32:35], v[40:43], v[176:179]
	v_mfma_f32_16x16x32_f16 v[180:183], v[36:39], v[40:43], v[180:183]
	s_waitcnt lgkmcnt(2)
	v_mfma_f32_16x16x32_f16 v[184:187], v[16:19], v[44:47], v[184:187]
	v_mfma_f32_16x16x32_f16 v[188:191], v[20:23], v[44:47], v[188:191]
	v_mfma_f32_16x16x32_f16 v[192:195], v[24:27], v[44:47], v[192:195]
	v_mfma_f32_16x16x32_f16 v[196:199], v[28:31], v[44:47], v[196:199]
	v_mfma_f32_16x16x32_f16 v[200:203], v[32:35], v[44:47], v[200:203]
	v_mfma_f32_16x16x32_f16 v[204:207], v[36:39], v[44:47], v[204:207]
	s_waitcnt lgkmcnt(1)
	v_mfma_f32_16x16x32_f16 v[208:211], v[16:19], v[48:51], v[208:211]
	v_mfma_f32_16x16x32_f16 v[212:215], v[20:23], v[48:51], v[212:215]
	v_mfma_f32_16x16x32_f16 v[216:219], v[24:27], v[48:51], v[216:219]
	v_mfma_f32_16x16x32_f16 v[220:223], v[28:31], v[48:51], v[220:223]
	v_mfma_f32_16x16x32_f16 v[224:227], v[32:35], v[48:51], v[224:227]
	v_mfma_f32_16x16x32_f16 v[228:231], v[36:39], v[48:51], v[228:231]
	s_waitcnt lgkmcnt(0)
	v_mfma_f32_16x16x32_f16 v[232:235], v[16:19], v[52:55], v[232:235]
	v_mfma_f32_16x16x32_f16 v[236:239], v[20:23], v[52:55], v[236:239]
	v_mfma_f32_16x16x32_f16 v[240:243], v[24:27], v[52:55], v[240:243]
	v_mfma_f32_16x16x32_f16 v[244:247], v[28:31], v[52:55], v[244:247]
	v_mfma_f32_16x16x32_f16 v[248:251], v[32:35], v[52:55], v[248:251]
	v_mfma_f32_16x16x32_f16 v[252:255], v[36:39], v[52:55], v[252:255]
	s_setprio 0
	s_barrier
	ds_read_b128 v[16:19], v4 offset:40960
	ds_read_b128 v[20:23], v4 offset:41984
	ds_read_b128 v[24:27], v4 offset:43008
	ds_read_b128 v[28:31], v4 offset:44032
	ds_read_b128 v[32:35], v4 offset:45056
	ds_read_b128 v[36:39], v4 offset:46080
	ds_read_b128 v[40:43], v2 offset:40960
	ds_read_b128 v[44:47], v2 offset:41984
	ds_read_b128 v[48:51], v2 offset:43008
	ds_read_b128 v[52:55], v2 offset:44032
	s_cmp_eq_u32 s21, 11
	s_cbranch_scc1 .Lfc_nodma_h0
	s_add_u32 m0, s22, 0x0
	s_nop 0
	global_load_lds_dwordx4 v5, s[24:25]
	s_add_u32 m0, s22, 0xa000
	s_nop 0
	global_load_lds_dwordx4 v5, s[26:27]
	s_add_u32 m0, s22, 0x400
	s_nop 0
	global_load_lds_dwordx4 v6, s[24:25]
	s_add_u32 m0, s22, 0xa400
	s_nop 0
	global_load_lds_dwordx4 v6, s[26:27]
	s_add_u32 m0, s23, 0x0
	s_nop 0
	global_load_lds_dwordx4 v11, s[28:29]
	s_add_u32 m0, s23, 0xa000
	s_nop 0
	global_load_lds_dwordx4 v11, s[30:31]
	s_add_u32 m0, s23, 0x400
	s_nop 0
	global_load_lds_dwordx4 v11, s[32:33]
	s_add_u32 m0, s23, 0xa400
	s_nop 0
	global_load_lds_dwordx4 v11, s[34:35]
	s_add_u32 m0, s23, 0x800
	s_nop 0
	global_load_lds_dwordx4 v11, s[36:37]
	s_add_u32 m0, s23, 0xa800
	s_nop 0
	global_load_lds_dwordx4 v11, s[38:39]
	s_add_u32 s24, s24, 0x80
	s_addc_u32 s25, s25, 0
	s_add_u32 s26, s26, 0x80
	s_addc_u32 s27, s27, 0
	s_add_u32 s28, s28, 0x80
	s_addc_u32 s29, s29, 0
	s_add_u32 s30, s30, 0x80
	s_addc_u32 s31, s31, 0
	s_add_u32 s32, s32, 0x80
	s_addc_u32 s33, s33, 0
	s_add_u32 s34, s34, 0x80
	s_addc_u32 s35, s35, 0
	s_add_u32 s36, s36, 0x80
	s_addc_u32 s37, s37, 0
	s_add_u32 s38, s38, 0x80
	s_addc_u32 s39, s39, 0
.Lfc_nodma_h0:
	s_barrier
	s_waitcnt lgkmcnt(0)
	s_setprio 1
	v_mfma_f32_16x16x32_f16 v[64:67], v[16:19], v[40:43], v[64:67]
	v_mfma_f32_16x16x32_f16 v[68:71], v[20:23], v[40:43], v[68:71]
	v_mfma_f32_16x16x32_f16 v[72:75], v[24:27], v[40:43], v[72:75]
	v_mfma_f32_16x16x32_f16 v[76:79], v[28:31], v[40:43], v[76:79]
	v_mfma_f32_16x16x32_f16 v[80:83], v[32:35], v[40:43], v[80:83]
	v_mfma_f32_16x16x32_f16 v[84:87], v[36:39], v[40:43], v[84:87]
	v_mfma_f32_16x16x32_f16 v[88:91], v[16:19], v[44:47], v[88:91]
	ds_read_b128 v[40:43], v2 offset:45056
	v_mfma_f32_16x16x32_f16 v[92:95], v[20:23], v[44:47], v[92:95]
	v_mfma_f32_16x16x32_f16 v[96:99], v[24:27], v[44:47], v[96:99]
	v_mfma_f32_16x16x32_f16 v[100:103], v[28:31], v[44:47], v[100:103]
	v_mfma_f32_16x16x32_f16 v[104:107], v[32:35], v[44:47], v[104:107]
	v_mfma_f32_16x16x32_f16 v[108:111], v[36:39], v[44:47], v[108:111]
	v_mfma_f32_16x16x32_f16 v[112:115], v[16:19], v[48:51], v[112:115]
	ds_read_b128 v[44:47], v2 offset:46080
	v_mfma_f32_16x16x32_f16 v[116:119], v[20:23], v[48:51], v[116:119]
	v_mfma_f32_16x16x32_f16 v[120:123], v[24:27], v[48:51], v[120:123]
	v_mfma_f32_16x16x32_f16 v[124:127], v[28:31], v[48:51], v[124:127]
	v_mfma_f32_16x16x32_f16 v[128:131], v[32:35], v[48:51], v[128:131]
	v_mfma_f32_16x16x32_f16 v[132:135], v[36:39], v[48:51], v[132:135]
	v_mfma_f32_16x16x32_f16 v[136:139], v[16:19], v[52:55], v[136:139]
	ds_read_b128 v[48:51], v2 offset:47104
	v_mfma_f32_16x16x32_f16 v[140:143], v[20:23], v[52:55], v[140:143]
	v_mfma_f32_16x16x32_f16 v[144:147], v[24:27], v[52:55], v[144:147]
	v_mfma_f32_16x16x32_f16 v[148:151], v[28:31], v[52:55], v[148:151]
	v_mfma_f32_16x16x32_f16 v[152:155], v[32:35], v[52:55], v[152:155]
	v_mfma_f32_16x16x32_f16 v[156:159], v[36:39], v[52:55], v[156:159]
	s_waitcnt lgkmcnt(2)
	v_mfma_f32_16x16x32_f16 v[160:163], v[16:19], v[40:43], v[160:163]
	ds_read_b128 v[52:55], v2 offset:48128
	v_mfma_f32_16x16x32_f16 v[164:167], v[20:23], v[40:43], v[164:167]
	v_mfma_f32_16x16x32_f16 v[168:171], v[24:27], v[40:43], v[168:171]
	v_mfma_f32_16x16x32_f16 v[172:175], v[28:31], v[40:43], v[172:175]
	v_mfma_f32_16x16x32_f16 v[176:179], v[32:35], v[40:43], v[176:179]
	v_mfma_f32_16x16x32_f16 v[180:183], v[36:39], v[40:43], v[180:183]
	s_waitcnt lgkmcnt(2)
	v_mfma_f32_16x16x32_f16 v[184:187], v[16:19], v[44:47], v[184:187]
	v_mfma_f32_16x16x32_f16 v[188:191], v[20:23], v[44:47], v[188:191]
	v_mfma_f32_16x16x32_f16 v[192:195], v[24:27], v[44:47], v[192:195]
	v_mfma_f32_16x16x32_f16 v[196:199], v[28:31], v[44:47], v[196:199]
	v_mfma_f32_16x16x32_f16 v[200:203], v[32:35], v[44:47], v[200:203]
	v_mfma_f32_16x16x32_f16 v[204:207], v[36:39], v[44:47], v[204:207]
	s_waitcnt lgkmcnt(1)
	v_mfma_f32_16x16x32_f16 v[208:211], v[16:19], v[48:51], v[208:211]
	v_mfma_f32_16x16x32_f16 v[212:215], v[20:23], v[48:51], v[212:215]
	v_mfma_f32_16x16x32_f16 v[216:219], v[24:27], v[48:51], v[216:219]
	v_mfma_f32_16x16x32_f16 v[220:223], v[28:31], v[48:51], v[220:223]
	v_mfma_f32_16x16x32_f16 v[224:227], v[32:35], v[48:51], v[224:227]
	v_mfma_f32_16x16x32_f16 v[228:231], v[36:39], v[48:51], v[228:231]
	s_waitcnt lgkmcnt(0)
	v_mfma_f32_16x16x32_f16 v[232:235], v[16:19], v[52:55], v[232:235]
	v_mfma_f32_16x16x32_f16 v[236:239], v[20:23], v[52:55], v[236:239]
	v_mfma_f32_16x16x32_f16 v[240:243], v[24:27], v[52:55], v[240:243]
	v_mfma_f32_16x16x32_f16 v[244:247], v[28:31], v[52:55], v[244:247]
	v_mfma_f32_16x16x32_f16 v[248:251], v[32:35], v[52:55], v[248:251]
	v_mfma_f32_16x16x32_f16 v[252:255], v[36:39], v[52:55], v[252:255]
	s_setprio 0
	s_waitcnt vmcnt(0)
	s_barrier
	s_add_u32 s21, s21, 1
	s_cmp_lt_u32 s21, 12
	s_cbranch_scc1 .Lfc_h0_loop
	s_barrier
	s_branch .Lfc_epi

.Lfc_h1_loop:
	ds_read_b128 v[16:19], v3 offset:0
	ds_read_b128 v[20:23], v3 offset:1024
	ds_read_b128 v[24:27], v3 offset:2048
	ds_read_b128 v[28:31], v3 offset:3072
	ds_read_b128 v[32:35], v3 offset:4096
	ds_read_b128 v[36:39], v3 offset:5120
	ds_read_b128 v[40:43], v1 offset:0
	ds_read_b128 v[44:47], v1 offset:1024
	ds_read_b128 v[48:51], v1 offset:2048
	ds_read_b128 v[52:55], v1 offset:3072
	s_add_u32 m0, s22, 0x14000
	s_nop 0
	global_load_lds_dwordx4 v5, s[24:25]
	s_add_u32 m0, s22, 0x1e000
	s_nop 0
	global_load_lds_dwordx4 v5, s[26:27]
	s_add_u32 m0, s22, 0x14400
	s_nop 0
	global_load_lds_dwordx4 v6, s[24:25]
	s_add_u32 m0, s22, 0x1e400
	s_nop 0
	global_load_lds_dwordx4 v6, s[26:27]
	s_add_u32 m0, s23, 0x14000
	s_nop 0
	global_load_lds_dwordx4 v11, s[28:29]
	s_add_u32 m0, s23, 0x1e000
	s_nop 0
	global_load_lds_dwordx4 v11, s[30:31]
	s_add_u32 m0, s23, 0x14400
	s_nop 0
	global_load_lds_dwordx4 v11, s[32:33]
	s_add_u32 m0, s23, 0x1e400
	s_nop 0
	global_load_lds_dwordx4 v11, s[34:35]
	s_add_u32 m0, s23, 0x14800
	s_nop 0
	global_load_lds_dwordx4 v11, s[36:37]
	s_add_u32 m0, s23, 0x1e800
	s_nop 0
	global_load_lds_dwordx4 v11, s[38:39]
	s_add_u32 s28, s28, 0x80
	s_addc_u32 s29, s29, 0
	s_add_u32 s30, s30, 0x80
	s_addc_u32 s31, s31, 0
	s_add_u32 s32, s32, 0x80
	s_addc_u32 s33, s33, 0
	s_add_u32 s34, s34, 0x80
	s_addc_u32 s35, s35, 0
	s_add_u32 s36, s36, 0x80
	s_addc_u32 s37, s37, 0
	s_add_u32 s38, s38, 0x80
	s_addc_u32 s39, s39, 0
	s_cmp_eq_u32 s21, 3
	s_cbranch_scc1 .Lfc_sw_h1
	s_cmp_eq_u32 s21, 7
	s_cbranch_scc1 .Lfc_sw_h1
	s_add_u32 s24, s24, 0x80
	s_addc_u32 s25, s25, 0
	s_add_u32 s26, s26, 0x80
	s_addc_u32 s27, s27, 0
	s_branch .Lfc_swd_h1

.Lfc_swd_h1:
	s_barrier
	s_waitcnt lgkmcnt(0)
	s_setprio 1
	v_mfma_f32_16x16x32_f16 v[64:67], v[16:19], v[40:43], v[64:67]
	v_mfma_f32_16x16x32_f16 v[68:71], v[20:23], v[40:43], v[68:71]
	v_mfma_f32_16x16x32_f16 v[72:75], v[24:27], v[40:43], v[72:75]
	v_mfma_f32_16x16x32_f16 v[76:79], v[28:31], v[40:43], v[76:79]
	v_mfma_f32_16x16x32_f16 v[80:83], v[32:35], v[40:43], v[80:83]
	v_mfma_f32_16x16x32_f16 v[84:87], v[36:39], v[40:43], v[84:87]
	v_mfma_f32_16x16x32_f16 v[88:91], v[16:19], v[44:47], v[88:91]
	ds_read_b128 v[40:43], v1 offset:4096
	v_mfma_f32_16x16x32_f16 v[92:95], v[20:23], v[44:47], v[92:95]
	v_mfma_f32_16x16x32_f16 v[96:99], v[24:27], v[44:47], v[96:99]
	v_mfma_f32_16x16x32_f16 v[100:103], v[28:31], v[44:47], v[100:103]
	v_mfma_f32_16x16x32_f16 v[104:107], v[32:35], v[44:47], v[104:107]
	v_mfma_f32_16x16x32_f16 v[108:111], v[36:39], v[44:47], v[108:111]
	v_mfma_f32_16x16x32_f16 v[112:115], v[16:19], v[48:51], v[112:115]
	ds_read_b128 v[44:47], v1 offset:5120
	v_mfma_f32_16x16x32_f16 v[116:119], v[20:23], v[48:51], v[116:119]
	v_mfma_f32_16x16x32_f16 v[120:123], v[24:27], v[48:51], v[120:123]
	v_mfma_f32_16x16x32_f16 v[124:127], v[28:31], v[48:51], v[124:127]
	v_mfma_f32_16x16x32_f16 v[128:131], v[32:35], v[48:51], v[128:131]
	v_mfma_f32_16x16x32_f16 v[132:135], v[36:39], v[48:51], v[132:135]
	v_mfma_f32_16x16x32_f16 v[136:139], v[16:19], v[52:55], v[136:139]
	ds_read_b128 v[48:51], v1 offset:6144
	v_mfma_f32_16x16x32_f16 v[140:143], v[20:23], v[52:55], v[140:143]
	v_mfma_f32_16x16x32_f16 v[144:147], v[24:27], v[52:55], v[144:147]
	v_mfma_f32_16x16x32_f16 v[148:151], v[28:31], v[52:55], v[148:151]
	v_mfma_f32_16x16x32_f16 v[152:155], v[32:35], v[52:55], v[152:155]
	v_mfma_f32_16x16x32_f16 v[156:159], v[36:39], v[52:55], v[156:159]
	s_waitcnt lgkmcnt(2)
	v_mfma_f32_16x16x32_f16 v[160:163], v[16:19], v[40:43], v[160:163]
	ds_read_b128 v[52:55], v1 offset:7168
	v_mfma_f32_16x16x32_f16 v[164:167], v[20:23], v[40:43], v[164:167]
	v_mfma_f32_16x16x32_f16 v[168:171], v[24:27], v[40:43], v[168:171]
	v_mfma_f32_16x16x32_f16 v[172:175], v[28:31], v[40:43], v[172:175]
	v_mfma_f32_16x16x32_f16 v[176:179], v[32:35], v[40:43], v[176:179]
	v_mfma_f32_16x16x32_f16 v[180:183], v[36:39], v[40:43], v[180:183]
	s_waitcnt lgkmcnt(2)
	v_mfma_f32_16x16x32_f16 v[184:187], v[16:19], v[44:47], v[184:187]
	v_mfma_f32_16x16x32_f16 v[188:191], v[20:23], v[44:47], v[188:191]
	v_mfma_f32_16x16x32_f16 v[192:195], v[24:27], v[44:47], v[192:195]
	v_mfma_f32_16x16x32_f16 v[196:199], v[28:31], v[44:47], v[196:199]
	v_mfma_f32_16x16x32_f16 v[200:203], v[32:35], v[44:47], v[200:203]
	v_mfma_f32_16x16x32_f16 v[204:207], v[36:39], v[44:47], v[204:207]
	s_waitcnt lgkmcnt(1)
	v_mfma_f32_16x16x32_f16 v[208:211], v[16:19], v[48:51], v[208:211]
	v_mfma_f32_16x16x32_f16 v[212:215], v[20:23], v[48:51], v[212:215]
	v_mfma_f32_16x16x32_f16 v[216:219], v[24:27], v[48:51], v[216:219]
	v_mfma_f32_16x16x32_f16 v[220:223], v[28:31], v[48:51], v[220:223]
	v_mfma_f32_16x16x32_f16 v[224:227], v[32:35], v[48:51], v[224:227]
	v_mfma_f32_16x16x32_f16 v[228:231], v[36:39], v[48:51], v[228:231]
	s_waitcnt lgkmcnt(0)
	v_mfma_f32_16x16x32_f16 v[232:235], v[16:19], v[52:55], v[232:235]
	v_mfma_f32_16x16x32_f16 v[236:239], v[20:23], v[52:55], v[236:239]
	v_mfma_f32_16x16x32_f16 v[240:243], v[24:27], v[52:55], v[240:243]
	v_mfma_f32_16x16x32_f16 v[244:247], v[28:31], v[52:55], v[244:247]
	v_mfma_f32_16x16x32_f16 v[248:251], v[32:35], v[52:55], v[248:251]
	v_mfma_f32_16x16x32_f16 v[252:255], v[36:39], v[52:55], v[252:255]
	s_setprio 0
	s_barrier
	ds_read_b128 v[16:19], v3 offset:40960
	ds_read_b128 v[20:23], v3 offset:41984
	ds_read_b128 v[24:27], v3 offset:43008
	ds_read_b128 v[28:31], v3 offset:44032
	ds_read_b128 v[32:35], v3 offset:45056
	ds_read_b128 v[36:39], v3 offset:46080
	ds_read_b128 v[40:43], v1 offset:40960
	ds_read_b128 v[44:47], v1 offset:41984
	ds_read_b128 v[48:51], v1 offset:43008
	ds_read_b128 v[52:55], v1 offset:44032
	s_waitcnt vmcnt(0)
	s_barrier
	s_waitcnt lgkmcnt(0)
	s_setprio 1
	v_mfma_f32_16x16x32_f16 v[64:67], v[16:19], v[40:43], v[64:67]
	v_mfma_f32_16x16x32_f16 v[68:71], v[20:23], v[40:43], v[68:71]
	v_mfma_f32_16x16x32_f16 v[72:75], v[24:27], v[40:43], v[72:75]
	v_mfma_f32_16x16x32_f16 v[76:79], v[28:31], v[40:43], v[76:79]
	v_mfma_f32_16x16x32_f16 v[80:83], v[32:35], v[40:43], v[80:83]
	v_mfma_f32_16x16x32_f16 v[84:87], v[36:39], v[40:43], v[84:87]
	v_mfma_f32_16x16x32_f16 v[88:91], v[16:19], v[44:47], v[88:91]
	ds_read_b128 v[40:43], v1 offset:45056
	v_mfma_f32_16x16x32_f16 v[92:95], v[20:23], v[44:47], v[92:95]
	v_mfma_f32_16x16x32_f16 v[96:99], v[24:27], v[44:47], v[96:99]
	v_mfma_f32_16x16x32_f16 v[100:103], v[28:31], v[44:47], v[100:103]
	v_mfma_f32_16x16x32_f16 v[104:107], v[32:35], v[44:47], v[104:107]
	v_mfma_f32_16x16x32_f16 v[108:111], v[36:39], v[44:47], v[108:111]
	v_mfma_f32_16x16x32_f16 v[112:115], v[16:19], v[48:51], v[112:115]
	ds_read_b128 v[44:47], v1 offset:46080
	v_mfma_f32_16x16x32_f16 v[116:119], v[20:23], v[48:51], v[116:119]
	v_mfma_f32_16x16x32_f16 v[120:123], v[24:27], v[48:51], v[120:123]
	v_mfma_f32_16x16x32_f16 v[124:127], v[28:31], v[48:51], v[124:127]
	v_mfma_f32_16x16x32_f16 v[128:131], v[32:35], v[48:51], v[128:131]
	v_mfma_f32_16x16x32_f16 v[132:135], v[36:39], v[48:51], v[132:135]
	v_mfma_f32_16x16x32_f16 v[136:139], v[16:19], v[52:55], v[136:139]
	ds_read_b128 v[48:51], v1 offset:47104
	v_mfma_f32_16x16x32_f16 v[140:143], v[20:23], v[52:55], v[140:143]
	v_mfma_f32_16x16x32_f16 v[144:147], v[24:27], v[52:55], v[144:147]
	v_mfma_f32_16x16x32_f16 v[148:151], v[28:31], v[52:55], v[148:151]
	v_mfma_f32_16x16x32_f16 v[152:155], v[32:35], v[52:55], v[152:155]
	v_mfma_f32_16x16x32_f16 v[156:159], v[36:39], v[52:55], v[156:159]
	s_waitcnt lgkmcnt(2)
	v_mfma_f32_16x16x32_f16 v[160:163], v[16:19], v[40:43], v[160:163]
	ds_read_b128 v[52:55], v1 offset:48128
	v_mfma_f32_16x16x32_f16 v[164:167], v[20:23], v[40:43], v[164:167]
	v_mfma_f32_16x16x32_f16 v[168:171], v[24:27], v[40:43], v[168:171]
	v_mfma_f32_16x16x32_f16 v[172:175], v[28:31], v[40:43], v[172:175]
	v_mfma_f32_16x16x32_f16 v[176:179], v[32:35], v[40:43], v[176:179]
	v_mfma_f32_16x16x32_f16 v[180:183], v[36:39], v[40:43], v[180:183]
	s_waitcnt lgkmcnt(2)
	v_mfma_f32_16x16x32_f16 v[184:187], v[16:19], v[44:47], v[184:187]
	v_mfma_f32_16x16x32_f16 v[188:191], v[20:23], v[44:47], v[188:191]
	v_mfma_f32_16x16x32_f16 v[192:195], v[24:27], v[44:47], v[192:195]
	v_mfma_f32_16x16x32_f16 v[196:199], v[28:31], v[44:47], v[196:199]
	v_mfma_f32_16x16x32_f16 v[200:203], v[32:35], v[44:47], v[200:203]
	v_mfma_f32_16x16x32_f16 v[204:207], v[36:39], v[44:47], v[204:207]
	s_waitcnt lgkmcnt(1)
	v_mfma_f32_16x16x32_f16 v[208:211], v[16:19], v[48:51], v[208:211]
	v_mfma_f32_16x16x32_f16 v[212:215], v[20:23], v[48:51], v[212:215]
	v_mfma_f32_16x16x32_f16 v[216:219], v[24:27], v[48:51], v[216:219]
	v_mfma_f32_16x16x32_f16 v[220:223], v[28:31], v[48:51], v[220:223]
	v_mfma_f32_16x16x32_f16 v[224:227], v[32:35], v[48:51], v[224:227]
	v_mfma_f32_16x16x32_f16 v[228:231], v[36:39], v[48:51], v[228:231]
	s_waitcnt lgkmcnt(0)
	v_mfma_f32_16x16x32_f16 v[232:235], v[16:19], v[52:55], v[232:235]
	v_mfma_f32_16x16x32_f16 v[236:239], v[20:23], v[52:55], v[236:239]
	v_mfma_f32_16x16x32_f16 v[240:243], v[24:27], v[52:55], v[240:243]
	v_mfma_f32_16x16x32_f16 v[244:247], v[28:31], v[52:55], v[244:247]
	v_mfma_f32_16x16x32_f16 v[248:251], v[32:35], v[52:55], v[248:251]
	v_mfma_f32_16x16x32_f16 v[252:255], v[36:39], v[52:55], v[252:255]
	s_setprio 0
	s_barrier
	ds_read_b128 v[16:19], v4 offset:0
	ds_read_b128 v[20:23], v4 offset:1024
	ds_read_b128 v[24:27], v4 offset:2048
	ds_read_b128 v[28:31], v4 offset:3072
	ds_read_b128 v[32:35], v4 offset:4096
	ds_read_b128 v[36:39], v4 offset:5120
	ds_read_b128 v[40:43], v2 offset:0
	ds_read_b128 v[44:47], v2 offset:1024
	ds_read_b128 v[48:51], v2 offset:2048
	ds_read_b128 v[52:55], v2 offset:3072
	s_cmp_eq_u32 s21, 11
	s_cbranch_scc1 .Lfc_nodma_h1
	s_add_u32 m0, s22, 0x0
	s_nop 0
	global_load_lds_dwordx4 v5, s[24:25]
	s_add_u32 m0, s22, 0xa000
	s_nop 0
	global_load_lds_dwordx4 v5, s[26:27]
	s_add_u32 m0, s22, 0x400
	s_nop 0
	global_load_lds_dwordx4 v6, s[24:25]
	s_add_u32 m0, s22, 0xa400
	s_nop 0
	global_load_lds_dwordx4 v6, s[26:27]
	s_add_u32 m0, s23, 0x0
	s_nop 0
	global_load_lds_dwordx4 v11, s[28:29]
	s_add_u32 m0, s23, 0xa000
	s_nop 0
	global_load_lds_dwordx4 v11, s[30:31]
	s_add_u32 m0, s23, 0x400
	s_nop 0
	global_load_lds_dwordx4 v11, s[32:33]
	s_add_u32 m0, s23, 0xa400
	s_nop 0
	global_load_lds_dwordx4 v11, s[34:35]
	s_add_u32 m0, s23, 0x800
	s_nop 0
	global_load_lds_dwordx4 v11, s[36:37]
	s_add_u32 m0, s23, 0xa800
	s_nop 0
	global_load_lds_dwordx4 v11, s[38:39]
	s_add_u32 s24, s24, 0x80
	s_addc_u32 s25, s25, 0
	s_add_u32 s26, s26, 0x80
	s_addc_u32 s27, s27, 0
	s_add_u32 s28, s28, 0x80
	s_addc_u32 s29, s29, 0
	s_add_u32 s30, s30, 0x80
	s_addc_u32 s31, s31, 0
	s_add_u32 s32, s32, 0x80
	s_addc_u32 s33, s33, 0
	s_add_u32 s34, s34, 0x80
	s_addc_u32 s35, s35, 0
	s_add_u32 s36, s36, 0x80
	s_addc_u32 s37, s37, 0
	s_add_u32 s38, s38, 0x80
	s_addc_u32 s39, s39, 0
.Lfc_nodma_h1:
	s_barrier
	s_waitcnt lgkmcnt(0)
	s_setprio 1
	v_mfma_f32_16x16x32_f16 v[64:67], v[16:19], v[40:43], v[64:67]
	v_mfma_f32_16x16x32_f16 v[68:71], v[20:23], v[40:43], v[68:71]
	v_mfma_f32_16x16x32_f16 v[72:75], v[24:27], v[40:43], v[72:75]
	v_mfma_f32_16x16x32_f16 v[76:79], v[28:31], v[40:43], v[76:79]
	v_mfma_f32_16x16x32_f16 v[80:83], v[32:35], v[40:43], v[80:83]
	v_mfma_f32_16x16x32_f16 v[84:87], v[36:39], v[40:43], v[84:87]
	v_mfma_f32_16x16x32_f16 v[88:91], v[16:19], v[44:47], v[88:91]
	ds_read_b128 v[40:43], v2 offset:4096
	v_mfma_f32_16x16x32_f16 v[92:95], v[20:23], v[44:47], v[92:95]
	v_mfma_f32_16x16x32_f16 v[96:99], v[24:27], v[44:47], v[96:99]
	v_mfma_f32_16x16x32_f16 v[100:103], v[28:31], v[44:47], v[100:103]
	v_mfma_f32_16x16x32_f16 v[104:107], v[32:35], v[44:47], v[104:107]
	v_mfma_f32_16x16x32_f16 v[108:111], v[36:39], v[44:47], v[108:111]
	v_mfma_f32_16x16x32_f16 v[112:115], v[16:19], v[48:51], v[112:115]
	ds_read_b128 v[44:47], v2 offset:5120
	v_mfma_f32_16x16x32_f16 v[116:119], v[20:23], v[48:51], v[116:119]
	v_mfma_f32_16x16x32_f16 v[120:123], v[24:27], v[48:51], v[120:123]
	v_mfma_f32_16x16x32_f16 v[124:127], v[28:31], v[48:51], v[124:127]
	v_mfma_f32_16x16x32_f16 v[128:131], v[32:35], v[48:51], v[128:131]
	v_mfma_f32_16x16x32_f16 v[132:135], v[36:39], v[48:51], v[132:135]
	v_mfma_f32_16x16x32_f16 v[136:139], v[16:19], v[52:55], v[136:139]
	ds_read_b128 v[48:51], v2 offset:6144
	v_mfma_f32_16x16x32_f16 v[140:143], v[20:23], v[52:55], v[140:143]
	v_mfma_f32_16x16x32_f16 v[144:147], v[24:27], v[52:55], v[144:147]
	v_mfma_f32_16x16x32_f16 v[148:151], v[28:31], v[52:55], v[148:151]
	v_mfma_f32_16x16x32_f16 v[152:155], v[32:35], v[52:55], v[152:155]
	v_mfma_f32_16x16x32_f16 v[156:159], v[36:39], v[52:55], v[156:159]
	s_waitcnt lgkmcnt(2)
	v_mfma_f32_16x16x32_f16 v[160:163], v[16:19], v[40:43], v[160:163]
	ds_read_b128 v[52:55], v2 offset:7168
	v_mfma_f32_16x16x32_f16 v[164:167], v[20:23], v[40:43], v[164:167]
	v_mfma_f32_16x16x32_f16 v[168:171], v[24:27], v[40:43], v[168:171]
	v_mfma_f32_16x16x32_f16 v[172:175], v[28:31], v[40:43], v[172:175]
	v_mfma_f32_16x16x32_f16 v[176:179], v[32:35], v[40:43], v[176:179]
	v_mfma_f32_16x16x32_f16 v[180:183], v[36:39], v[40:43], v[180:183]
	s_waitcnt lgkmcnt(2)
	v_mfma_f32_16x16x32_f16 v[184:187], v[16:19], v[44:47], v[184:187]
	v_mfma_f32_16x16x32_f16 v[188:191], v[20:23], v[44:47], v[188:191]
	v_mfma_f32_16x16x32_f16 v[192:195], v[24:27], v[44:47], v[192:195]
	v_mfma_f32_16x16x32_f16 v[196:199], v[28:31], v[44:47], v[196:199]
	v_mfma_f32_16x16x32_f16 v[200:203], v[32:35], v[44:47], v[200:203]
	v_mfma_f32_16x16x32_f16 v[204:207], v[36:39], v[44:47], v[204:207]
	s_waitcnt lgkmcnt(1)
	v_mfma_f32_16x16x32_f16 v[208:211], v[16:19], v[48:51], v[208:211]
	v_mfma_f32_16x16x32_f16 v[212:215], v[20:23], v[48:51], v[212:215]
	v_mfma_f32_16x16x32_f16 v[216:219], v[24:27], v[48:51], v[216:219]
	v_mfma_f32_16x16x32_f16 v[220:223], v[28:31], v[48:51], v[220:223]
	v_mfma_f32_16x16x32_f16 v[224:227], v[32:35], v[48:51], v[224:227]
	v_mfma_f32_16x16x32_f16 v[228:231], v[36:39], v[48:51], v[228:231]
	s_waitcnt lgkmcnt(0)
	v_mfma_f32_16x16x32_f16 v[232:235], v[16:19], v[52:55], v[232:235]
	v_mfma_f32_16x16x32_f16 v[236:239], v[20:23], v[52:55], v[236:239]
	v_mfma_f32_16x16x32_f16 v[240:243], v[24:27], v[52:55], v[240:243]
	v_mfma_f32_16x16x32_f16 v[244:247], v[28:31], v[52:55], v[244:247]
	v_mfma_f32_16x16x32_f16 v[248:251], v[32:35], v[52:55], v[248:251]
	v_mfma_f32_16x16x32_f16 v[252:255], v[36:39], v[52:55], v[252:255]
	s_setprio 0
	s_barrier
	ds_read_b128 v[16:19], v4 offset:40960
	ds_read_b128 v[20:23], v4 offset:41984
	ds_read_b128 v[24:27], v4 offset:43008
	ds_read_b128 v[28:31], v4 offset:44032
	ds_read_b128 v[32:35], v4 offset:45056
	ds_read_b128 v[36:39], v4 offset:46080
	ds_read_b128 v[40:43], v2 offset:40960
	ds_read_b128 v[44:47], v2 offset:41984
	ds_read_b128 v[48:51], v2 offset:43008
	ds_read_b128 v[52:55], v2 offset:44032
	s_waitcnt vmcnt(0)
	s_barrier
	s_waitcnt lgkmcnt(0)
	s_setprio 1
	v_mfma_f32_16x16x32_f16 v[64:67], v[16:19], v[40:43], v[64:67]
	v_mfma_f32_16x16x32_f16 v[68:71], v[20:23], v[40:43], v[68:71]
	v_mfma_f32_16x16x32_f16 v[72:75], v[24:27], v[40:43], v[72:75]
	v_mfma_f32_16x16x32_f16 v[76:79], v[28:31], v[40:43], v[76:79]
	v_mfma_f32_16x16x32_f16 v[80:83], v[32:35], v[40:43], v[80:83]
	v_mfma_f32_16x16x32_f16 v[84:87], v[36:39], v[40:43], v[84:87]
	v_mfma_f32_16x16x32_f16 v[88:91], v[16:19], v[44:47], v[88:91]
	ds_read_b128 v[40:43], v2 offset:45056
	v_mfma_f32_16x16x32_f16 v[92:95], v[20:23], v[44:47], v[92:95]
	v_mfma_f32_16x16x32_f16 v[96:99], v[24:27], v[44:47], v[96:99]
	v_mfma_f32_16x16x32_f16 v[100:103], v[28:31], v[44:47], v[100:103]
	v_mfma_f32_16x16x32_f16 v[104:107], v[32:35], v[44:47], v[104:107]
	v_mfma_f32_16x16x32_f16 v[108:111], v[36:39], v[44:47], v[108:111]
	v_mfma_f32_16x16x32_f16 v[112:115], v[16:19], v[48:51], v[112:115]
	ds_read_b128 v[44:47], v2 offset:46080
	v_mfma_f32_16x16x32_f16 v[116:119], v[20:23], v[48:51], v[116:119]
	v_mfma_f32_16x16x32_f16 v[120:123], v[24:27], v[48:51], v[120:123]
	v_mfma_f32_16x16x32_f16 v[124:127], v[28:31], v[48:51], v[124:127]
	v_mfma_f32_16x16x32_f16 v[128:131], v[32:35], v[48:51], v[128:131]
	v_mfma_f32_16x16x32_f16 v[132:135], v[36:39], v[48:51], v[132:135]
	v_mfma_f32_16x16x32_f16 v[136:139], v[16:19], v[52:55], v[136:139]
	ds_read_b128 v[48:51], v2 offset:47104
	v_mfma_f32_16x16x32_f16 v[140:143], v[20:23], v[52:55], v[140:143]
	v_mfma_f32_16x16x32_f16 v[144:147], v[24:27], v[52:55], v[144:147]
	v_mfma_f32_16x16x32_f16 v[148:151], v[28:31], v[52:55], v[148:151]
	v_mfma_f32_16x16x32_f16 v[152:155], v[32:35], v[52:55], v[152:155]
	v_mfma_f32_16x16x32_f16 v[156:159], v[36:39], v[52:55], v[156:159]
	s_waitcnt lgkmcnt(2)
	v_mfma_f32_16x16x32_f16 v[160:163], v[16:19], v[40:43], v[160:163]
	ds_read_b128 v[52:55], v2 offset:48128
	v_mfma_f32_16x16x32_f16 v[164:167], v[20:23], v[40:43], v[164:167]
	v_mfma_f32_16x16x32_f16 v[168:171], v[24:27], v[40:43], v[168:171]
	v_mfma_f32_16x16x32_f16 v[172:175], v[28:31], v[40:43], v[172:175]
	v_mfma_f32_16x16x32_f16 v[176:179], v[32:35], v[40:43], v[176:179]
	v_mfma_f32_16x16x32_f16 v[180:183], v[36:39], v[40:43], v[180:183]
	s_waitcnt lgkmcnt(2)
	v_mfma_f32_16x16x32_f16 v[184:187], v[16:19], v[44:47], v[184:187]
	v_mfma_f32_16x16x32_f16 v[188:191], v[20:23], v[44:47], v[188:191]
	v_mfma_f32_16x16x32_f16 v[192:195], v[24:27], v[44:47], v[192:195]
	v_mfma_f32_16x16x32_f16 v[196:199], v[28:31], v[44:47], v[196:199]
	v_mfma_f32_16x16x32_f16 v[200:203], v[32:35], v[44:47], v[200:203]
	v_mfma_f32_16x16x32_f16 v[204:207], v[36:39], v[44:47], v[204:207]
	s_waitcnt lgkmcnt(1)
	v_mfma_f32_16x16x32_f16 v[208:211], v[16:19], v[48:51], v[208:211]
	v_mfma_f32_16x16x32_f16 v[212:215], v[20:23], v[48:51], v[212:215]
	v_mfma_f32_16x16x32_f16 v[216:219], v[24:27], v[48:51], v[216:219]
	v_mfma_f32_16x16x32_f16 v[220:223], v[28:31], v[48:51], v[220:223]
	v_mfma_f32_16x16x32_f16 v[224:227], v[32:35], v[48:51], v[224:227]
	v_mfma_f32_16x16x32_f16 v[228:231], v[36:39], v[48:51], v[228:231]
	s_waitcnt lgkmcnt(0)
	v_mfma_f32_16x16x32_f16 v[232:235], v[16:19], v[52:55], v[232:235]
	v_mfma_f32_16x16x32_f16 v[236:239], v[20:23], v[52:55], v[236:239]
	v_mfma_f32_16x16x32_f16 v[240:243], v[24:27], v[52:55], v[240:243]
	v_mfma_f32_16x16x32_f16 v[244:247], v[28:31], v[52:55], v[244:247]
	v_mfma_f32_16x16x32_f16 v[248:251], v[32:35], v[52:55], v[248:251]
	v_mfma_f32_16x16x32_f16 v[252:255], v[36:39], v[52:55], v[252:255]
	s_setprio 0
	s_barrier
	s_add_u32 s21, s21, 1
	s_cmp_lt_u32 s21, 12
	s_cbranch_scc1 .Lfc_h1_loop
.Lfc_epi:
	s_nop 7
	v_and_b32_e32 v12, 63, v0
	v_and_b32_e32 v13, 15, v0
	v_lshrrev_b32_e32 v14, 4, v12
	s_mul_i32 s42, s20, 0x180
	s_mul_i32 s43, s18, 96
	s_add_u32 s42, s42, s43
	v_lshl_add_u32 v15, v14, 2, s42
	v_lshlrev_b32_e32 v15, 2, v15
	global_load_dwordx4 v[16:19], v15, s[10:11] offset:0
	global_load_dwordx4 v[20:23], v15, s[10:11] offset:64
	global_load_dwordx4 v[24:27], v15, s[10:11] offset:128
	global_load_dwordx4 v[28:31], v15, s[10:11] offset:192
	global_load_dwordx4 v[32:35], v15, s[10:11] offset:256
	global_load_dwordx4 v[36:39], v15, s[10:11] offset:320
	v_mul_u32_u24_e32 v11, 0x1800, v13
	v_add_u32_e32 v11, v11, v15
	v_mov_b32_e32 v40, 0
	v_mov_b32_e32 v41, 0
	v_mov_b32_e32 v42, 0
	v_mov_b32_e32 v43, 0
	v_mov_b32_e32 v44, 0
	v_mov_b32_e32 v45, 0
	v_mov_b32_e32 v46, 0
	v_mov_b32_e32 v47, 0
	v_mov_b32_e32 v48, 0
	v_mov_b32_e32 v49, 0
	v_mov_b32_e32 v50, 0
	v_mov_b32_e32 v51, 0
	v_mov_b32_e32 v52, 0
	v_mov_b32_e32 v53, 0
	v_mov_b32_e32 v54, 0
	v_mov_b32_e32 v55, 0
	v_mov_b32_e32 v56, 0
	v_mov_b32_e32 v57, 0
	v_mov_b32_e32 v58, 0
	v_mov_b32_e32 v59, 0
	v_mov_b32_e32 v60, 0
	v_mov_b32_e32 v61, 0
	v_mov_b32_e32 v62, 0
	v_mov_b32_e32 v63, 0
	s_mov_b32 exec_lo, 0xff00ff
	s_mov_b32 exec_hi, 0xff00ff
	global_load_dwordx4 v[40:43], v11, s[12:13] offset:0
	global_load_dwordx4 v[44:47], v11, s[12:13] offset:64
	global_load_dwordx4 v[48:51], v11, s[12:13] offset:128
	global_load_dwordx4 v[52:55], v11, s[12:13] offset:192
	global_load_dwordx4 v[56:59], v11, s[12:13] offset:256
	global_load_dwordx4 v[60:63], v11, s[12:13] offset:320
	s_mov_b64 exec, -1
	s_lshl_b32 s42, s18, 8
	s_lshl_b32 s43, s17, 7
	s_add_u32 s42, s42, s43
	v_add_u32_e32 v1, s42, v13
	v_lshlrev_b32_e32 v1, 5, v1
	v_lshl_add_u32 v1, v14, 4, v1
	v_lshlrev_b32_e32 v2, 4, v12
	v_add_u32_e32 v2, 0x10000, v2
	v_cmp_gt_u32_e32 vcc, 2, v14
	s_nop 1
	v_cndmask_b32_e32 v1, v2, v1, vcc
	s_waitcnt vmcnt(0)
	v_cvt_pk_f16_f32 v40, v40, v41
	v_cvt_pk_f16_f32 v41, v42, v43
	v_cvt_pk_f16_f32 v42, v44, v45
	v_cvt_pk_f16_f32 v43, v46, v47
	v_cvt_pk_f16_f32 v48, v48, v49
	v_cvt_pk_f16_f32 v49, v50, v51
	v_cvt_pk_f16_f32 v50, v52, v53
	v_cvt_pk_f16_f32 v51, v54, v55
	v_cvt_pk_f16_f32 v56, v56, v57
	v_cvt_pk_f16_f32 v57, v58, v59
	v_cvt_pk_f16_f32 v58, v60, v61
	v_cvt_pk_f16_f32 v59, v62, v63
	v_pk_add_f32 v[64:65], v[64:65], v[16:17]
	v_pk_add_f32 v[66:67], v[66:67], v[18:19]
	v_pk_add_f32 v[68:69], v[68:69], v[20:21]
	v_pk_add_f32 v[70:71], v[70:71], v[22:23]
	v_max_f32_e32 v64, 0, v64
	v_max_f32_e32 v65, 0, v65
	v_max_f32_e32 v66, 0, v66
	v_max_f32_e32 v67, 0, v67
	v_max_f32_e32 v68, 0, v68
	v_max_f32_e32 v69, 0, v69
	v_max_f32_e32 v70, 0, v70
	v_max_f32_e32 v71, 0, v71
	v_cvt_pk_f16_f32 v44, v64, v65
	v_cvt_pk_f16_f32 v45, v66, v67
	v_cvt_pk_f16_f32 v46, v68, v69
	v_cvt_pk_f16_f32 v47, v70, v71
	s_nop 1
	v_mfma_f32_16x16x32_f16 v[60:63], v[40:43], v[44:47], 0
	v_pk_add_f32 v[72:73], v[72:73], v[24:25]
	v_pk_add_f32 v[74:75], v[74:75], v[26:27]
	v_pk_add_f32 v[76:77], v[76:77], v[28:29]
	v_pk_add_f32 v[78:79], v[78:79], v[30:31]
	v_max_f32_e32 v72, 0, v72
	v_max_f32_e32 v73, 0, v73
	v_max_f32_e32 v74, 0, v74
	v_max_f32_e32 v75, 0, v75
	v_max_f32_e32 v76, 0, v76
	v_max_f32_e32 v77, 0, v77
	v_max_f32_e32 v78, 0, v78
	v_max_f32_e32 v79, 0, v79
	v_cvt_pk_f16_f32 v52, v72, v73
	v_cvt_pk_f16_f32 v53, v74, v75
	v_cvt_pk_f16_f32 v54, v76, v77
	v_cvt_pk_f16_f32 v55, v78, v79
	s_nop 1
	v_mfma_f32_16x16x32_f16 v[60:63], v[48:51], v[52:55], v[60:63]
	v_pk_add_f32 v[80:81], v[80:81], v[32:33]
	v_pk_add_f32 v[82:83], v[82:83], v[34:35]
	v_pk_add_f32 v[84:85], v[84:85], v[36:37]
	v_pk_add_f32 v[86:87], v[86:87], v[38:39]
	v_max_f32_e32 v80, 0, v80
	v_max_f32_e32 v81, 0, v81
	v_max_f32_e32 v82, 0, v82
	v_max_f32_e32 v83, 0, v83
	v_max_f32_e32 v84, 0, v84
	v_max_f32_e32 v85, 0, v85
	v_max_f32_e32 v86, 0, v86
	v_max_f32_e32 v87, 0, v87
	v_cvt_pk_f16_f32 v44, v80, v81
	v_cvt_pk_f16_f32 v45, v82, v83
	v_cvt_pk_f16_f32 v46, v84, v85
	v_cvt_pk_f16_f32 v47, v86, v87
	s_nop 1
	v_mfma_f32_16x16x32_f16 v[60:63], v[56:59], v[44:47], v[60:63]
	v_pk_add_f32 v[88:89], v[88:89], v[16:17]
	v_pk_add_f32 v[90:91], v[90:91], v[18:19]
	v_pk_add_f32 v[92:93], v[92:93], v[20:21]
	v_pk_add_f32 v[94:95], v[94:95], v[22:23]
	v_max_f32_e32 v88, 0, v88
	v_max_f32_e32 v89, 0, v89
	v_max_f32_e32 v90, 0, v90
	v_max_f32_e32 v91, 0, v91
	v_max_f32_e32 v92, 0, v92
	v_max_f32_e32 v93, 0, v93
	v_max_f32_e32 v94, 0, v94
	v_max_f32_e32 v95, 0, v95
	v_cvt_pk_f16_f32 v52, v88, v89
	v_cvt_pk_f16_f32 v53, v90, v91
	v_cvt_pk_f16_f32 v54, v92, v93
	v_cvt_pk_f16_f32 v55, v94, v95
	s_nop 1
	v_mfma_f32_16x16x32_f16 v[12:15], v[40:43], v[52:55], 0
	v_pk_add_f32 v[96:97], v[96:97], v[24:25]
	v_pk_add_f32 v[98:99], v[98:99], v[26:27]
	v_pk_add_f32 v[100:101], v[100:101], v[28:29]
	v_pk_add_f32 v[102:103], v[102:103], v[30:31]
	v_max_f32_e32 v96, 0, v96
	v_max_f32_e32 v97, 0, v97
	v_max_f32_e32 v98, 0, v98
	v_max_f32_e32 v99, 0, v99
	v_max_f32_e32 v100, 0, v100
	v_max_f32_e32 v101, 0, v101
	v_max_f32_e32 v102, 0, v102
	v_max_f32_e32 v103, 0, v103
	v_cvt_pk_f16_f32 v44, v96, v97
	v_cvt_pk_f16_f32 v45, v98, v99
	v_cvt_pk_f16_f32 v46, v100, v101
	v_cvt_pk_f16_f32 v47, v102, v103
	s_nop 1
	v_mfma_f32_16x16x32_f16 v[12:15], v[48:51], v[44:47], v[12:15]
	ds_write_b128 v1, v[60:63] offset:0
	v_pk_add_f32 v[104:105], v[104:105], v[32:33]
	v_pk_add_f32 v[106:107], v[106:107], v[34:35]
	v_pk_add_f32 v[108:109], v[108:109], v[36:37]
	v_pk_add_f32 v[110:111], v[110:111], v[38:39]
	v_max_f32_e32 v104, 0, v104
	v_max_f32_e32 v105, 0, v105
	v_max_f32_e32 v106, 0, v106
	v_max_f32_e32 v107, 0, v107
	v_max_f32_e32 v108, 0, v108
	v_max_f32_e32 v109, 0, v109
	v_max_f32_e32 v110, 0, v110
	v_max_f32_e32 v111, 0, v111
	v_cvt_pk_f16_f32 v52, v104, v105
	v_cvt_pk_f16_f32 v53, v106, v107
	v_cvt_pk_f16_f32 v54, v108, v109
	v_cvt_pk_f16_f32 v55, v110, v111
	s_nop 1
	v_mfma_f32_16x16x32_f16 v[12:15], v[56:59], v[52:55], v[12:15]
	v_pk_add_f32 v[112:113], v[112:113], v[16:17]
	v_pk_add_f32 v[114:115], v[114:115], v[18:19]
	v_pk_add_f32 v[116:117], v[116:117], v[20:21]
	v_pk_add_f32 v[118:119], v[118:119], v[22:23]
	v_max_f32_e32 v112, 0, v112
	v_max_f32_e32 v113, 0, v113
	v_max_f32_e32 v114, 0, v114
	v_max_f32_e32 v115, 0, v115
	v_max_f32_e32 v116, 0, v116
	v_max_f32_e32 v117, 0, v117
	v_max_f32_e32 v118, 0, v118
	v_max_f32_e32 v119, 0, v119
	v_cvt_pk_f16_f32 v44, v112, v113
	v_cvt_pk_f16_f32 v45, v114, v115
	v_cvt_pk_f16_f32 v46, v116, v117
	v_cvt_pk_f16_f32 v47, v118, v119
	s_nop 1
	v_mfma_f32_16x16x32_f16 v[60:63], v[40:43], v[44:47], 0
	v_pk_add_f32 v[120:121], v[120:121], v[24:25]
	v_pk_add_f32 v[122:123], v[122:123], v[26:27]
	v_pk_add_f32 v[124:125], v[124:125], v[28:29]
	v_pk_add_f32 v[126:127], v[126:127], v[30:31]
	v_max_f32_e32 v120, 0, v120
	v_max_f32_e32 v121, 0, v121
	v_max_f32_e32 v122, 0, v122
	v_max_f32_e32 v123, 0, v123
	v_max_f32_e32 v124, 0, v124
	v_max_f32_e32 v125, 0, v125
	v_max_f32_e32 v126, 0, v126
	v_max_f32_e32 v127, 0, v127
	v_cvt_pk_f16_f32 v52, v120, v121
	v_cvt_pk_f16_f32 v53, v122, v123
	v_cvt_pk_f16_f32 v54, v124, v125
	v_cvt_pk_f16_f32 v55, v126, v127
	s_nop 1
	v_mfma_f32_16x16x32_f16 v[60:63], v[48:51], v[52:55], v[60:63]
	ds_write_b128 v1, v[12:15] offset:512
	v_pk_add_f32 v[128:129], v[128:129], v[32:33]
	v_pk_add_f32 v[130:131], v[130:131], v[34:35]
	v_pk_add_f32 v[132:133], v[132:133], v[36:37]
	v_pk_add_f32 v[134:135], v[134:135], v[38:39]
	v_max_f32_e32 v128, 0, v128
	v_max_f32_e32 v129, 0, v129
	v_max_f32_e32 v130, 0, v130
	v_max_f32_e32 v131, 0, v131
	v_max_f32_e32 v132, 0, v132
	v_max_f32_e32 v133, 0, v133
	v_max_f32_e32 v134, 0, v134
	v_max_f32_e32 v135, 0, v135
	v_cvt_pk_f16_f32 v44, v128, v129
	v_cvt_pk_f16_f32 v45, v130, v131
	v_cvt_pk_f16_f32 v46, v132, v133
	v_cvt_pk_f16_f32 v47, v134, v135
	s_nop 1
	v_mfma_f32_16x16x32_f16 v[60:63], v[56:59], v[44:47], v[60:63]
	v_pk_add_f32 v[136:137], v[136:137], v[16:17]
	v_pk_add_f32 v[138:139], v[138:139], v[18:19]
	v_pk_add_f32 v[140:141], v[140:141], v[20:21]
	v_pk_add_f32 v[142:143], v[142:143], v[22:23]
	v_max_f32_e32 v136, 0, v136
	v_max_f32_e32 v137, 0, v137
	v_max_f32_e32 v138, 0, v138
	v_max_f32_e32 v139, 0, v139
	v_max_f32_e32 v140, 0, v140
	v_max_f32_e32 v141, 0, v141
	v_max_f32_e32 v142, 0, v142
	v_max_f32_e32 v143, 0, v143
	v_cvt_pk_f16_f32 v52, v136, v137
	v_cvt_pk_f16_f32 v53, v138, v139
	v_cvt_pk_f16_f32 v54, v140, v141
	v_cvt_pk_f16_f32 v55, v142, v143
	s_nop 1
	v_mfma_f32_16x16x32_f16 v[12:15], v[40:43], v[52:55], 0
	v_pk_add_f32 v[144:145], v[144:145], v[24:25]
	v_pk_add_f32 v[146:147], v[146:147], v[26:27]
	v_pk_add_f32 v[148:149], v[148:149], v[28:29]
	v_pk_add_f32 v[150:151], v[150:151], v[30:31]
	v_max_f32_e32 v144, 0, v144
	v_max_f32_e32 v145, 0, v145
	v_max_f32_e32 v146, 0, v146
	v_max_f32_e32 v147, 0, v147
	v_max_f32_e32 v148, 0, v148
	v_max_f32_e32 v149, 0, v149
	v_max_f32_e32 v150, 0, v150
	v_max_f32_e32 v151, 0, v151
	v_cvt_pk_f16_f32 v44, v144, v145
	v_cvt_pk_f16_f32 v45, v146, v147
	v_cvt_pk_f16_f32 v46, v148, v149
	v_cvt_pk_f16_f32 v47, v150, v151
	s_nop 1
	v_mfma_f32_16x16x32_f16 v[12:15], v[48:51], v[44:47], v[12:15]
	ds_write_b128 v1, v[60:63] offset:1024
	v_pk_add_f32 v[152:153], v[152:153], v[32:33]
	v_pk_add_f32 v[154:155], v[154:155], v[34:35]
	v_pk_add_f32 v[156:157], v[156:157], v[36:37]
	v_pk_add_f32 v[158:159], v[158:159], v[38:39]
	v_max_f32_e32 v152, 0, v152
	v_max_f32_e32 v153, 0, v153
	v_max_f32_e32 v154, 0, v154
	v_max_f32_e32 v155, 0, v155
	v_max_f32_e32 v156, 0, v156
	v_max_f32_e32 v157, 0, v157
	v_max_f32_e32 v158, 0, v158
	v_max_f32_e32 v159, 0, v159
	v_cvt_pk_f16_f32 v52, v152, v153
	v_cvt_pk_f16_f32 v53, v154, v155
	v_cvt_pk_f16_f32 v54, v156, v157
	v_cvt_pk_f16_f32 v55, v158, v159
	s_nop 1
	v_mfma_f32_16x16x32_f16 v[12:15], v[56:59], v[52:55], v[12:15]
	v_pk_add_f32 v[160:161], v[160:161], v[16:17]
	v_pk_add_f32 v[162:163], v[162:163], v[18:19]
	v_pk_add_f32 v[164:165], v[164:165], v[20:21]
	v_pk_add_f32 v[166:167], v[166:167], v[22:23]
	v_max_f32_e32 v160, 0, v160
	v_max_f32_e32 v161, 0, v161
	v_max_f32_e32 v162, 0, v162
	v_max_f32_e32 v163, 0, v163
	v_max_f32_e32 v164, 0, v164
	v_max_f32_e32 v165, 0, v165
	v_max_f32_e32 v166, 0, v166
	v_max_f32_e32 v167, 0, v167
	v_cvt_pk_f16_f32 v44, v160, v161
	v_cvt_pk_f16_f32 v45, v162, v163
	v_cvt_pk_f16_f32 v46, v164, v165
	v_cvt_pk_f16_f32 v47, v166, v167
	s_nop 1
	v_mfma_f32_16x16x32_f16 v[60:63], v[40:43], v[44:47], 0
	v_pk_add_f32 v[168:169], v[168:169], v[24:25]
	v_pk_add_f32 v[170:171], v[170:171], v[26:27]
	v_pk_add_f32 v[172:173], v[172:173], v[28:29]
	v_pk_add_f32 v[174:175], v[174:175], v[30:31]
	v_max_f32_e32 v168, 0, v168
	v_max_f32_e32 v169, 0, v169
	v_max_f32_e32 v170, 0, v170
	v_max_f32_e32 v171, 0, v171
	v_max_f32_e32 v172, 0, v172
	v_max_f32_e32 v173, 0, v173
	v_max_f32_e32 v174, 0, v174
	v_max_f32_e32 v175, 0, v175
	v_cvt_pk_f16_f32 v52, v168, v169
	v_cvt_pk_f16_f32 v53, v170, v171
	v_cvt_pk_f16_f32 v54, v172, v173
	v_cvt_pk_f16_f32 v55, v174, v175
	s_nop 1
	v_mfma_f32_16x16x32_f16 v[60:63], v[48:51], v[52:55], v[60:63]
	ds_write_b128 v1, v[12:15] offset:1536
	v_pk_add_f32 v[176:177], v[176:177], v[32:33]
	v_pk_add_f32 v[178:179], v[178:179], v[34:35]
	v_pk_add_f32 v[180:181], v[180:181], v[36:37]
	v_pk_add_f32 v[182:183], v[182:183], v[38:39]
	v_max_f32_e32 v176, 0, v176
	v_max_f32_e32 v177, 0, v177
	v_max_f32_e32 v178, 0, v178
	v_max_f32_e32 v179, 0, v179
	v_max_f32_e32 v180, 0, v180
	v_max_f32_e32 v181, 0, v181
	v_max_f32_e32 v182, 0, v182
	v_max_f32_e32 v183, 0, v183
	v_cvt_pk_f16_f32 v44, v176, v177
	v_cvt_pk_f16_f32 v45, v178, v179
	v_cvt_pk_f16_f32 v46, v180, v181
	v_cvt_pk_f16_f32 v47, v182, v183
	s_nop 1
	v_mfma_f32_16x16x32_f16 v[60:63], v[56:59], v[44:47], v[60:63]
	v_pk_add_f32 v[184:185], v[184:185], v[16:17]
	v_pk_add_f32 v[186:187], v[186:187], v[18:19]
	v_pk_add_f32 v[188:189], v[188:189], v[20:21]
	v_pk_add_f32 v[190:191], v[190:191], v[22:23]
	v_max_f32_e32 v184, 0, v184
	v_max_f32_e32 v185, 0, v185
	v_max_f32_e32 v186, 0, v186
	v_max_f32_e32 v187, 0, v187
	v_max_f32_e32 v188, 0, v188
	v_max_f32_e32 v189, 0, v189
	v_max_f32_e32 v190, 0, v190
	v_max_f32_e32 v191, 0, v191
	v_cvt_pk_f16_f32 v52, v184, v185
	v_cvt_pk_f16_f32 v53, v186, v187
	v_cvt_pk_f16_f32 v54, v188, v189
	v_cvt_pk_f16_f32 v55, v190, v191
	s_nop 1
	v_mfma_f32_16x16x32_f16 v[12:15], v[40:43], v[52:55], 0
	v_pk_add_f32 v[192:193], v[192:193], v[24:25]
	v_pk_add_f32 v[194:195], v[194:195], v[26:27]
	v_pk_add_f32 v[196:197], v[196:197], v[28:29]
	v_pk_add_f32 v[198:199], v[198:199], v[30:31]
	v_max_f32_e32 v192, 0, v192
	v_max_f32_e32 v193, 0, v193
	v_max_f32_e32 v194, 0, v194
	v_max_f32_e32 v195, 0, v195
	v_max_f32_e32 v196, 0, v196
	v_max_f32_e32 v197, 0, v197
	v_max_f32_e32 v198, 0, v198
	v_max_f32_e32 v199, 0, v199
	v_cvt_pk_f16_f32 v44, v192, v193
	v_cvt_pk_f16_f32 v45, v194, v195
	v_cvt_pk_f16_f32 v46, v196, v197
	v_cvt_pk_f16_f32 v47, v198, v199
	s_nop 1
	v_mfma_f32_16x16x32_f16 v[12:15], v[48:51], v[44:47], v[12:15]
	ds_write_b128 v1, v[60:63] offset:2048
	v_pk_add_f32 v[200:201], v[200:201], v[32:33]
	v_pk_add_f32 v[202:203], v[202:203], v[34:35]
	v_pk_add_f32 v[204:205], v[204:205], v[36:37]
	v_pk_add_f32 v[206:207], v[206:207], v[38:39]
	v_max_f32_e32 v200, 0, v200
	v_max_f32_e32 v201, 0, v201
	v_max_f32_e32 v202, 0, v202
	v_max_f32_e32 v203, 0, v203
	v_max_f32_e32 v204, 0, v204
	v_max_f32_e32 v205, 0, v205
	v_max_f32_e32 v206, 0, v206
	v_max_f32_e32 v207, 0, v207
	v_cvt_pk_f16_f32 v52, v200, v201
	v_cvt_pk_f16_f32 v53, v202, v203
	v_cvt_pk_f16_f32 v54, v204, v205
	v_cvt_pk_f16_f32 v55, v206, v207
	s_nop 1
	v_mfma_f32_16x16x32_f16 v[12:15], v[56:59], v[52:55], v[12:15]
	v_pk_add_f32 v[208:209], v[208:209], v[16:17]
	v_pk_add_f32 v[210:211], v[210:211], v[18:19]
	v_pk_add_f32 v[212:213], v[212:213], v[20:21]
	v_pk_add_f32 v[214:215], v[214:215], v[22:23]
	v_max_f32_e32 v208, 0, v208
	v_max_f32_e32 v209, 0, v209
	v_max_f32_e32 v210, 0, v210
	v_max_f32_e32 v211, 0, v211
	v_max_f32_e32 v212, 0, v212
	v_max_f32_e32 v213, 0, v213
	v_max_f32_e32 v214, 0, v214
	v_max_f32_e32 v215, 0, v215
	v_cvt_pk_f16_f32 v44, v208, v209
	v_cvt_pk_f16_f32 v45, v210, v211
	v_cvt_pk_f16_f32 v46, v212, v213
	v_cvt_pk_f16_f32 v47, v214, v215
	s_nop 1
	v_mfma_f32_16x16x32_f16 v[60:63], v[40:43], v[44:47], 0
	v_pk_add_f32 v[216:217], v[216:217], v[24:25]
	v_pk_add_f32 v[218:219], v[218:219], v[26:27]
	v_pk_add_f32 v[220:221], v[220:221], v[28:29]
	v_pk_add_f32 v[222:223], v[222:223], v[30:31]
	v_max_f32_e32 v216, 0, v216
	v_max_f32_e32 v217, 0, v217
	v_max_f32_e32 v218, 0, v218
	v_max_f32_e32 v219, 0, v219
	v_max_f32_e32 v220, 0, v220
	v_max_f32_e32 v221, 0, v221
	v_max_f32_e32 v222, 0, v222
	v_max_f32_e32 v223, 0, v223
	v_cvt_pk_f16_f32 v52, v216, v217
	v_cvt_pk_f16_f32 v53, v218, v219
	v_cvt_pk_f16_f32 v54, v220, v221
	v_cvt_pk_f16_f32 v55, v222, v223
	s_nop 1
	v_mfma_f32_16x16x32_f16 v[60:63], v[48:51], v[52:55], v[60:63]
	ds_write_b128 v1, v[12:15] offset:2560
	v_pk_add_f32 v[224:225], v[224:225], v[32:33]
	v_pk_add_f32 v[226:227], v[226:227], v[34:35]
	v_pk_add_f32 v[228:229], v[228:229], v[36:37]
	v_pk_add_f32 v[230:231], v[230:231], v[38:39]
	v_max_f32_e32 v224, 0, v224
	v_max_f32_e32 v225, 0, v225
	v_max_f32_e32 v226, 0, v226
	v_max_f32_e32 v227, 0, v227
	v_max_f32_e32 v228, 0, v228
	v_max_f32_e32 v229, 0, v229
	v_max_f32_e32 v230, 0, v230
	v_max_f32_e32 v231, 0, v231
	v_cvt_pk_f16_f32 v44, v224, v225
	v_cvt_pk_f16_f32 v45, v226, v227
	v_cvt_pk_f16_f32 v46, v228, v229
	v_cvt_pk_f16_f32 v47, v230, v231
	s_nop 1
	v_mfma_f32_16x16x32_f16 v[60:63], v[56:59], v[44:47], v[60:63]
	v_pk_add_f32 v[232:233], v[232:233], v[16:17]
	v_pk_add_f32 v[234:235], v[234:235], v[18:19]
	v_pk_add_f32 v[236:237], v[236:237], v[20:21]
	v_pk_add_f32 v[238:239], v[238:239], v[22:23]
	v_max_f32_e32 v232, 0, v232
	v_max_f32_e32 v233, 0, v233
	v_max_f32_e32 v234, 0, v234
	v_max_f32_e32 v235, 0, v235
	v_max_f32_e32 v236, 0, v236
	v_max_f32_e32 v237, 0, v237
	v_max_f32_e32 v238, 0, v238
	v_max_f32_e32 v239, 0, v239
	v_cvt_pk_f16_f32 v52, v232, v233
	v_cvt_pk_f16_f32 v53, v234, v235
	v_cvt_pk_f16_f32 v54, v236, v237
	v_cvt_pk_f16_f32 v55, v238, v239
	s_nop 1
	v_mfma_f32_16x16x32_f16 v[12:15], v[40:43], v[52:55], 0
	v_pk_add_f32 v[240:241], v[240:241], v[24:25]
	v_pk_add_f32 v[242:243], v[242:243], v[26:27]
	v_pk_add_f32 v[244:245], v[244:245], v[28:29]
	v_pk_add_f32 v[246:247], v[246:247], v[30:31]
	v_max_f32_e32 v240, 0, v240
	v_max_f32_e32 v241, 0, v241
	v_max_f32_e32 v242, 0, v242
	v_max_f32_e32 v243, 0, v243
	v_max_f32_e32 v244, 0, v244
	v_max_f32_e32 v245, 0, v245
	v_max_f32_e32 v246, 0, v246
	v_max_f32_e32 v247, 0, v247
	v_cvt_pk_f16_f32 v44, v240, v241
	v_cvt_pk_f16_f32 v45, v242, v243
	v_cvt_pk_f16_f32 v46, v244, v245
	v_cvt_pk_f16_f32 v47, v246, v247
	s_nop 1
	v_mfma_f32_16x16x32_f16 v[12:15], v[48:51], v[44:47], v[12:15]
	ds_write_b128 v1, v[60:63] offset:3072
	v_pk_add_f32 v[248:249], v[248:249], v[32:33]
	v_pk_add_f32 v[250:251], v[250:251], v[34:35]
	v_pk_add_f32 v[252:253], v[252:253], v[36:37]
	v_pk_add_f32 v[254:255], v[254:255], v[38:39]
	v_max_f32_e32 v248, 0, v248
	v_max_f32_e32 v249, 0, v249
	v_max_f32_e32 v250, 0, v250
	v_max_f32_e32 v251, 0, v251
	v_max_f32_e32 v252, 0, v252
	v_max_f32_e32 v253, 0, v253
	v_max_f32_e32 v254, 0, v254
	v_max_f32_e32 v255, 0, v255
	v_cvt_pk_f16_f32 v52, v248, v249
	v_cvt_pk_f16_f32 v53, v250, v251
	v_cvt_pk_f16_f32 v54, v252, v253
	v_cvt_pk_f16_f32 v55, v254, v255
	s_nop 1
	v_mfma_f32_16x16x32_f16 v[12:15], v[56:59], v[52:55], v[12:15]
	s_nop 7
	s_nop 1
	ds_write_b128 v1, v[12:15] offset:3584
	s_waitcnt lgkmcnt(0)
	s_barrier
	v_lshrrev_b32_e32 v2, 1, v0
	v_and_b32_e32 v3, 1, v0
	v_lshlrev_b32_e32 v4, 5, v2
	v_lshl_add_u32 v4, v3, 4, v4
	ds_read_b128 v[16:19], v4
	ds_read_b128 v[20:23], v4 offset:8192
	ds_read_b128 v[24:27], v4 offset:16384
	ds_read_b128 v[28:31], v4 offset:24576
	s_lshl_b32 s42, s20, 20
	s_lshl_b32 s43, s19, 13
	s_add_u32 s42, s42, s43
	s_add_u32 s14, s14, s42
	s_addc_u32 s15, s15, 0
	s_add_u32 s44, s14, 0x80000
	s_addc_u32 s45, s15, 0
	s_waitcnt lgkmcnt(0)
	v_pk_add_f32 v[16:17], v[16:17], v[20:21]
	v_pk_add_f32 v[18:19], v[18:19], v[22:23]
	v_pk_add_f32 v[24:25], v[24:25], v[28:29]
	v_pk_add_f32 v[26:27], v[26:27], v[30:31]
	global_store_dwordx4 v4, v[16:19], s[14:15]
	global_store_dwordx4 v4, v[24:27], s[44:45]
	s_endpgm
	.p2align	8

	.amdhsa_kernel _ZN12_GLOBAL__N_14k_fcEPKtPKiS1_PKfS5_Pf
		.amdhsa_group_segment_fixed_size 0
		.amdhsa_private_segment_fixed_size 0
		.amdhsa_kernarg_size 48
		.amdhsa_user_sgpr_count 2
		.amdhsa_user_sgpr_dispatch_ptr 0
		.amdhsa_user_sgpr_queue_ptr 0
		.amdhsa_user_sgpr_kernarg_segment_ptr 1
		.amdhsa_user_sgpr_dispatch_id 0
		.amdhsa_user_sgpr_kernarg_preload_length 0
		.amdhsa_user_sgpr_kernarg_preload_offset 0
		.amdhsa_user_sgpr_private_segment_size 0
		.amdhsa_uses_dynamic_stack 0
		.amdhsa_enable_private_segment 0
		.amdhsa_system_sgpr_workgroup_id_x 1
		.amdhsa_system_sgpr_workgroup_id_y 0
		.amdhsa_system_sgpr_workgroup_id_z 0
		.amdhsa_system_sgpr_workgroup_info 0
		.amdhsa_system_vgpr_workitem_id 0
		.amdhsa_next_free_vgpr 256
		.amdhsa_next_free_sgpr 56
		.amdhsa_accum_offset 256
		.amdhsa_reserve_vcc 1
		.amdhsa_float_round_mode_32 0
		.amdhsa_float_round_mode_16_64 0
		.amdhsa_float_denorm_mode_32 3
		.amdhsa_float_denorm_mode_16_64 3
		.amdhsa_dx10_clamp 1
		.amdhsa_ieee_mode 1
		.amdhsa_fp16_overflow 0
		.amdhsa_tg_split 0
		.amdhsa_exception_fp_ieee_invalid_op 0
		.amdhsa_exception_fp_denorm_src 0
		.amdhsa_exception_fp_ieee_div_zero 0
		.amdhsa_exception_fp_ieee_overflow 0
		.amdhsa_exception_fp_ieee_underflow 0
		.amdhsa_exception_fp_ieee_inexact 0
		.amdhsa_exception_int_div_zero 0
	.end_amdhsa_kernel

amdhsa.kernels:
  - .agpr_count:     0
    .args:
      - .actual_access:  read_only
        .address_space:  global
        .offset:         0
        .size:           8
        .value_kind:     global_buffer
      - .actual_access:  read_only
        .address_space:  global
        .offset:         8
        .size:           8
        .value_kind:     global_buffer
      - .actual_access:  read_only
        .address_space:  global
        .offset:         16
        .size:           8
        .value_kind:     global_buffer
      - .actual_access:  read_only
        .address_space:  global
        .offset:         24
        .size:           8
        .value_kind:     global_buffer
      - .actual_access:  write_only
        .address_space:  global
        .offset:         32
        .size:           8
        .value_kind:     global_buffer
      - .actual_access:  write_only
        .address_space:  global
        .offset:         40
        .size:           8
        .value_kind:     global_buffer
      - .actual_access:  write_only
        .address_space:  global
        .offset:         48
        .size:           8
        .value_kind:     global_buffer
    .group_segment_fixed_size: 0
    .kernarg_segment_align: 8
    .kernarg_segment_size: 56
    .language:       OpenCL C
    .language_version:
      - 2
      - 0
    .max_flat_workgroup_size: 256
    .name:           _ZN12_GLOBAL__N_16k_prepEPKiPKfS3_S3_PtS4_Pf
    .private_segment_fixed_size: 0
    .sgpr_count:     18
    .sgpr_spill_count: 0
    .symbol:         _ZN12_GLOBAL__N_16k_prepEPKiPKfS3_S3_PtS4_Pf.kd
    .uniform_work_group_size: 1
    .uses_dynamic_stack: false
    .vgpr_count:     16
    .vgpr_spill_count: 0
    .wavefront_size: 64
  - .agpr_count:     0
    .args:
      - .actual_access:  read_only
        .address_space:  global
        .offset:         0
        .size:           8
        .value_kind:     global_buffer
      - .actual_access:  read_only
        .address_space:  global
        .offset:         8
        .size:           8
        .value_kind:     global_buffer
      - .actual_access:  write_only
        .address_space:  global
        .offset:         16
        .size:           8
        .value_kind:     global_buffer
    .group_segment_fixed_size: 0
    .kernarg_segment_align: 8
    .kernarg_segment_size: 24
    .language:       OpenCL C
    .language_version:
      - 2
      - 0
    .max_flat_workgroup_size: 256
    .name:           _ZN12_GLOBAL__N_17k_finalEPKfS1_Pf
    .private_segment_fixed_size: 0
    .sgpr_count:     18
    .sgpr_spill_count: 0
    .symbol:         _ZN12_GLOBAL__N_17k_finalEPKfS1_Pf.kd
    .uniform_work_group_size: 1
    .uses_dynamic_stack: false
    .vgpr_count:     38
    .vgpr_spill_count: 0
    .wavefront_size: 64
  - .agpr_count:     0
    .args:
      - .address_space:  global
        .offset:         0
        .size:           8
        .value_kind:     global_buffer
      - .address_space:  global
        .offset:         8
        .size:           8
        .value_kind:     global_buffer
      - .actual_access:  read_only
        .address_space:  global
        .offset:         16
        .size:           8
        .value_kind:     global_buffer
      - .actual_access:  read_only
        .address_space:  global
        .offset:         24
        .size:           8
        .value_kind:     global_buffer
      - .actual_access:  write_only
        .address_space:  global
        .offset:         32
        .size:           8
        .value_kind:     global_buffer
      - .address_space:  global
        .offset:         40
        .size:           8
        .value_kind:     global_buffer
      - .actual_access:  write_only
        .address_space:  global
        .offset:         48
        .size:           8
        .value_kind:     global_buffer
    .group_segment_fixed_size: 0
    .kernarg_segment_align: 8
    .kernarg_segment_size: 56
    .language:       OpenCL C
    .language_version:
      - 2
      - 0
    .max_flat_workgroup_size: 512
    .name:           _ZN12_GLOBAL__N_110k_convpoolEPKtS1_PKfPKiPtS3_S6_
    .private_segment_fixed_size: 0
    .sgpr_count:     54
    .sgpr_spill_count: 0
    .symbol:         _ZN12_GLOBAL__N_110k_convpoolEPKtS1_PKfPKiPtS3_S6_.kd
    .uniform_work_group_size: 1
    .uses_dynamic_stack: false
    .vgpr_count:     200
    .vgpr_spill_count: 0
    .wavefront_size: 64
  - .agpr_count:     0
    .args:
      - .address_space:  global
        .offset:         0
        .size:           8
        .value_kind:     global_buffer
      - .address_space:  global
        .offset:         8
        .size:           8
        .value_kind:     global_buffer
      - .address_space:  global
        .offset:         16
        .size:           8
        .value_kind:     global_buffer
      - .address_space:  global
        .offset:         24
        .size:           8
        .value_kind:     global_buffer
      - .address_space:  global
        .offset:         32
        .size:           8
        .value_kind:     global_buffer
      - .address_space:  global
        .offset:         40
        .size:           8
        .value_kind:     global_buffer
    .group_segment_fixed_size: 0
    .kernarg_segment_align: 8
    .kernarg_segment_size: 48
    .language:       OpenCL C
    .language_version:
      - 2
      - 0
    .max_flat_workgroup_size: 512
    .name:           _ZN12_GLOBAL__N_14k_fcEPKtPKiS1_PKfS5_Pf
    .private_segment_fixed_size: 0
    .sgpr_count:     62
    .sgpr_spill_count: 0
    .symbol:         _ZN12_GLOBAL__N_14k_fcEPKtPKiS1_PKfS5_Pf.kd
    .uniform_work_group_size: 1
    .uses_dynamic_stack: false
    .vgpr_count:     256
    .vgpr_spill_count: 0
    .wavefront_size: 64
